# expert-weight conversion: nt loads + conflict-free LDS write mapping (row=(lane>>3)+8i, c4=8*wave+(lane&7))
# speedup vs baseline: 1.0008x; 1.0008x over previous
; #define LAS __attribute__((address_space(3)))
; DI void conv_load(const ConvItem& c, f32x4 (&v)[8], int tid) {
; #pragma unroll
;     for (int i = 0; i < 8; ++i) { const int idx = tid + 512 * i, row = idx >> 6, c4 = idx & 63; v[i] = *(const f32x4*)(c.src + (size_t)(c.k0 + row) * c.ld + c.n0 + 4 * c4); }
; }
; DI void conv_store(const ConvItem& c, const f32x4 (&v)[8], LAS float* scr, int tid) {
; #pragma unroll
;     for (int i = 0; i < 8; ++i) { const int idx = tid + 512 * i, row = idx >> 6, c4 = idx & 63; LAS float* d = scr + row * 257 + 4 * c4; d[0] = v[i].x; d[1] = v[i].y; d[2] = v[i].z; d[3] = v[i].w; }
;     ...
;         if (F.tid <= 128) { const int n = F.tid; int bucket;
;             if (n < 16) bucket = n; else { int lg = 16 + (int)(logf((float)n / 16.0f) / 2.0794415416798357f * 16.0f); bucket = lg < 31 ? lg : 31; }
;             lutv = relb[bucket * 8 + h]; }
.LBB0_1787:
	s_or_b64 exec, exec, s[0:1]
	v_lshlrev_b32_e32 v3, 2, v0
	s_waitcnt vmcnt(0)
	v_lshlrev_b32_e32 v13, 3, v0
	v_lshrrev_b32_e32 v146, 6, v147
	v_and_b32_e32 v163, 7, v147
	v_lshlrev_b32_e32 v146, 5, v146
	v_lshl_or_b32 v146, v163, 2, v146
	v_add_u32_e32 v161, 0x200, v147
	v_add_u32_e32 v176, 0x400, v147
	v_add_u32_e32 v178, 0x600, v147
	v_add_u32_e32 v180, 0x800, v147
	v_add_u32_e32 v182, 0xa00, v147
	v_add_u32_e32 v184, 0xc00, v147
	v_add_u32_e32 v186, 0xe00, v147
	v_mov_b32_e32 v3, s83
	s_movk_i32 s0, 0x404
	v_and_b32_e32 v148, 56, v13
	v_bfe_u32 v157, v147, 3, 3
	v_add_u32_e32 v163, 8, v157
	v_add_u32_e32 v177, 16, v157
	v_add_u32_e32 v179, 24, v157
	v_add_u32_e32 v181, 32, v157
	v_add_u32_e32 v183, 40, v157
	v_add_u32_e32 v185, 48, v157
	v_add_u32_e32 v187, 56, v157
	v_mad_u32_u24 v13, v148, s0, v3
	v_ashrrev_i32_e32 v150, 3, v147
	v_ashrrev_i32_e32 v152, 3, v161
	v_ashrrev_i32_e32 v154, 3, v176
	v_ashrrev_i32_e32 v156, 3, v178
	v_mul_lo_u32 v5, v157, s0
	v_mul_lo_u32 v6, v163, s0
	v_mul_lo_u32 v7, v177, s0
	v_mul_lo_u32 v8, v179, s0
	v_mul_lo_u32 v9, v181, s0
	v_mul_lo_u32 v10, v183, s0
	v_mul_lo_u32 v11, v185, s0
	v_mul_lo_u32 v12, v187, s0
	v_lshl_add_u32 v188, v150, 2, v13
	s_movk_i32 s0, 0xff00
	v_lshl_add_u32 v191, v152, 2, v13
	v_lshl_add_u32 v194, v154, 2, v13
	v_lshl_add_u32 v197, v156, 2, v13
	v_lshlrev_b32_e32 v13, 1, v156
	v_and_b32_e32 v198, 0x7f, v156
	v_add_u32_e32 v200, 0x100, v150
	v_and_b32_e32 v189, 0x7f, v150
	v_and_or_b32 v199, v13, s0, v198
	v_lshlrev_b32_e32 v13, 1, v200
	v_add_u32_e32 v206, 0x100, v152
	v_and_b32_e32 v192, 0x7f, v152
	v_and_or_b32 v201, v13, s0, v189
	v_lshlrev_b32_e32 v13, 1, v206
	v_add_u32_e32 v208, 0x100, v154
	v_and_b32_e32 v195, 0x7f, v154
	v_and_or_b32 v207, v13, s0, v192
	v_lshlrev_b32_e32 v13, 1, v208
	v_add_u32_e32 v210, 0x100, v156
	v_and_or_b32 v209, v13, s0, v195
	v_lshlrev_b32_e32 v13, 1, v210
	v_and_or_b32 v211, v13, s0, v198
	v_cvt_f32_u32_e32 v13, v147
	v_lshlrev_b32_e32 v14, 1, v150
	v_and_or_b32 v190, v14, s0, v189
	v_lshlrev_b32_e32 v14, 1, v152
	v_and_or_b32 v193, v14, s0, v192
	v_lshlrev_b32_e32 v14, 1, v154
	v_and_or_b32 v196, v14, s0, v195
	v_mul_f32_e32 v13, 0x3d800000, v13
	s_mov_b32 s0, 0x800000
	v_cmp_gt_f32_e32 vcc, s0, v13
	s_mov_b32 s0, 0x3f317217
	s_mov_b32 s4, 0x40051592
	v_cndmask_b32_e64 v14, 0, 32, vcc
	v_ldexp_f32 v13, v13, v14
	v_log_f32_e32 v13, v13
	v_ashrrev_i32_e32 v18, 2, v147
	s_add_i32 s33, s83, 0x11200
	s_add_i32 s64, s83, 0x11410
	v_mul_f32_e32 v16, 0x3f317217, v13
	v_fma_f32 v16, v13, s0, -v16
	v_fmac_f32_e32 v16, 0x3377d1cf, v13
	s_mov_b32 s0, 0x7f800000
	v_fmac_f32_e32 v16, 0x3f317217, v13
	v_cmp_lt_f32_e64 s[0:1], |v13|, s0
	s_add_i32 s65, s83, 0x11420
	v_and_b32_e32 v160, -2, v18
	v_cndmask_b32_e64 v13, v13, v16, s[0:1]
	v_mov_b32_e32 v16, 0x41b17218
	v_cndmask_b32_e32 v16, 0, v16, vcc
	v_sub_f32_e32 v13, v13, v16
	v_div_scale_f32 v16, s[0:1], s4, s4, v13
	v_rcp_f32_e32 v17, v16
	s_add_u32 s40, s94, 0xb200000
	s_addc_u32 s41, s95, 0
	s_add_u32 s66, s94, 0x23200000
	v_fma_f32 v18, -v16, v17, 1.0
	v_fmac_f32_e32 v17, v18, v17
	v_div_scale_f32 v18, vcc, v13, s4, v13
	v_mul_f32_e32 v19, v18, v17
	v_fma_f32 v20, -v16, v19, v18
	s_addc_u32 s67, s95, 0
	v_fmac_f32_e32 v19, v20, v17
	s_add_u32 s69, s94, 0x1a200000
	v_fma_f32 v16, -v16, v19, v18
	s_addc_u32 s89, s95, 0
	v_div_fmas_f32 v16, v16, v17, v19
	s_add_u32 s70, s94, 0x11200000
	v_div_fixup_f32 v13, v16, s4, v13
	s_addc_u32 s71, s95, 0
	s_lshl_b32 s44, s50, 5
	v_mul_f32_e32 v13, 0x41800000, v13
	s_add_i32 s72, s83, 0x11418
	s_lshl_b64 s[2:3], s[44:45], 19
	s_lshl_b64 s[42:43], s[44:45], 21
	s_add_i32 s73, s83, 0x11414
	s_add_i32 s74, s83, 0x11404
	v_cvt_i32_f32_e32 v13, v13
	s_add_u32 s75, s94, 0x12200000
	s_addc_u32 s76, s95, 0
	v_ashrrev_i32_e32 v151, 5, v0
	v_lshlrev_b32_e32 v14, 3, v147
	v_ashrrev_i32_e32 v16, 2, v161
	s_movk_i32 s0, 0x90
	v_and_b32_e32 v22, 64, v230
	s_add_u32 s77, s94, 0x16200000
	v_and_b32_e32 v149, 31, v0
	v_lshlrev_b32_e32 v2, 2, v151
	v_and_b32_e32 v15, 56, v14
	v_and_b32_e32 v162, -2, v16
	v_mul_lo_u32 v16, v150, s0
	v_mul_lo_u32 v17, v152, s0
	v_mul_lo_u32 v18, v154, s0
	v_mul_lo_u32 v19, v156, s0
	s_movk_i32 s0, 0x208
	v_xor_b32_e32 v21, 32, v230
	v_add_u32_e32 v22, 64, v22
	s_addc_u32 s78, s95, 0
	v_cmp_eq_u32_e64 s[10:11], 0, v0
	v_lshlrev_b32_e32 v142, 3, v151
	v_sub_u32_e32 v155, 0, v2
	v_cmp_gt_u32_e64 s[12:13], 32, v0
	v_mul_u32_u24_e32 v2, 0x208, v149
	v_lshlrev_b32_e32 v64, 1, v15
	v_min_i32_e32 v13, 15, v13
	v_lshlrev_b32_e32 v0, 4, v0
	v_mad_u32_u24 v3, v15, s0, v3
	v_ashrrev_i32_e32 v15, 1, v147
	v_ashrrev_i32_e32 v20, 1, v161
	v_cmp_lt_i32_e32 vcc, v21, v22
	s_add_i32 s0, s83, 0x9000
	v_ashrrev_i32_e32 v143, 31, v142
	v_lshlrev_b32_e32 v1, 4, v151
	v_lshl_add_u32 v4, v146, 2, s83
	s_movk_i32 s1, 0x81
	v_lshl_add_u32 v13, v13, 3, v232
	v_add_u32_e32 v16, s83, v16
	v_and_b32_e32 v0, 0x70, v0
	v_add_u32_e32 v17, s83, v17
	v_add_u32_e32 v18, s83, v18
	v_add_u32_e32 v19, s83, v19
	v_and_b32_e32 v15, -4, v15
	v_and_b32_e32 v20, -4, v20
	v_cndmask_b32_e32 v21, v230, v21, vcc
	v_cmp_gt_i32_e32 vcc, 16, v147
	v_add3_u32 v225, v2, v142, s0
	v_mul_u32_u24_e32 v2, 0x90, v149
	s_mov_b32 s79, 0
	v_lshl_add_u64 v[144:145], v[142:143], 1, s[40:41]
	v_lshl_add_u64 v[158:159], s[40:41], 0, v[64:65]
	v_cmp_gt_i32_e64 s[14:15], s1, v147
	v_lshl_or_b32 v212, s68, 5, v149
	v_lshl_add_u32 v213, v147, 2, s33
	v_cmp_eq_u32_e64 s[16:17], s1, v147
	v_lshlrev_b32_e32 v214, 2, v21
	v_cndmask_b32_e32 v215, v13, v14, vcc
	v_writelane_b32 v254, s83, 7
	v_add3_u32 v217, v2, v1, s83
	s_mov_b64 s[50:51], 0
	s_lshl_b64 s[46:47], s[2:3], 2
	v_add_u32_e32 v218, v16, v0
	v_add_u32_e32 v219, v17, v0
	v_add_u32_e32 v220, v18, v0
	v_add_u32_e32 v221, v19, v0
	v_add_u32_e32 v222, v3, v15
	v_add_u32_e32 v223, v3, v20
	v_add_u32_e32 v236, v4, v5
	v_add_u32_e32 v237, v4, v6
	v_add_u32_e32 v238, v4, v7
	v_add_u32_e32 v239, v4, v8
	v_add_u32_e32 v240, v4, v9
	v_add_u32_e32 v241, v4, v10
	v_add_u32_e32 v242, v4, v11
	v_add_u32_e32 v243, v4, v12
	s_mov_b64 s[48:49], 0
	s_branch .LBB0_1789

; DI ConvItem conv_item(int it, const float* wg, const float* wu, const float* wdn, bf16_t* we, bf16_t* wd) {
;     ConvItem c; const int e = it / 96; int r = it % 96;
;     if (r < 64) { const int up = r >> 5; r &= 31; c.src = (up ? wu : wg) + (size_t)e * DM * DEXP; c.ld = DEXP; c.k0 = (r >> 1) * 64; c.n0 = (r & 1) * 256; c.dst = we + (size_t)e * 1024 * 1024; c.Kd = 1024; c.mode = up; }
;     else { r -= 64; c.src = wdn + (size_t)e * DEXP * DM; c.ld = DM; c.k0 = (r >> 2) * 64; c.n0 = (r & 3) * 256; c.dst = wd + (size_t)e * 1024 * 512; c.Kd = 512; c.mode = 2; }
;     return c;
; }
; DI void conv_load(const ConvItem& c, f32x4 (&v)[8], int tid) {
; #pragma unroll
;     for (int i = 0; i < 8; ++i) { const int idx = tid + 512 * i, row = idx >> 6, c4 = idx & 63; v[i] = *(const f32x4*)(c.src + (size_t)(c.k0 + row) * c.ld + c.n0 + 4 * c4); }
.LBB0_1801:
	v_add_u32_e32 v0, s28, v157
	v_mad_i64_i32 v[0:1], s[18:19], s6, v0, 0
	v_add_u32_e32 v2, s28, v163
	v_lshl_add_u64 v[0:1], v[0:1], 2, s[2:3]
	v_lshlrev_b32_e32 v64, 2, v146
	v_mad_i64_i32 v[2:3], s[18:19], s6, v2, 0
	v_lshl_add_u64 v[0:1], v[0:1], 0, v[64:65]
	v_lshl_add_u64 v[2:3], v[2:3], 2, s[2:3]
	v_lshl_add_u64 v[2:3], v[2:3], 0, v[64:65]
	global_load_dwordx4 v[52:55], v[0:1], off nt
	global_load_dwordx4 v[48:51], v[2:3], off nt
	v_add_u32_e32 v0, s28, v177
	v_mad_i64_i32 v[0:1], s[18:19], s6, v0, 0
	v_add_u32_e32 v2, s28, v179
	v_lshl_add_u64 v[0:1], v[0:1], 2, s[2:3]
	v_mad_i64_i32 v[2:3], s[18:19], s6, v2, 0
	v_lshl_add_u64 v[0:1], v[0:1], 0, v[64:65]
	v_lshl_add_u64 v[2:3], v[2:3], 2, s[2:3]
	v_lshl_add_u64 v[2:3], v[2:3], 0, v[64:65]
	global_load_dwordx4 v[94:97], v[0:1], off nt
	global_load_dwordx4 v[56:59], v[2:3], off nt
	v_add_u32_e32 v0, s28, v181
	v_mad_i64_i32 v[0:1], s[18:19], s6, v0, 0
	v_add_u32_e32 v2, s28, v183
	v_lshl_add_u64 v[0:1], v[0:1], 2, s[2:3]
	v_mad_i64_i32 v[2:3], s[18:19], s6, v2, 0
	v_lshl_add_u64 v[0:1], v[0:1], 0, v[64:65]
	v_lshl_add_u64 v[2:3], v[2:3], 2, s[2:3]
	v_lshl_add_u64 v[2:3], v[2:3], 0, v[64:65]
	global_load_dwordx4 v[102:105], v[0:1], off nt
	global_load_dwordx4 v[98:101], v[2:3], off nt
	v_add_u32_e32 v0, s28, v185
	v_mad_i64_i32 v[0:1], s[18:19], s6, v0, 0
	v_add_u32_e32 v2, s28, v187
	v_lshl_add_u64 v[0:1], v[0:1], 2, s[2:3]
	v_mad_i64_i32 v[2:3], s[6:7], s6, v2, 0
	v_lshl_add_u64 v[0:1], v[0:1], 0, v[64:65]
	v_lshl_add_u64 v[2:3], v[2:3], 2, s[2:3]
	v_lshl_add_u64 v[2:3], v[2:3], 0, v[64:65]
	global_load_dwordx4 v[110:113], v[0:1], off nt
	global_load_dwordx4 v[106:109], v[2:3], off nt
	s_or_b32 s2, s56, 1
	s_mul_hi_i32 s3, s2, 0x2aaaaaab
	s_lshr_b32 s6, s3, 31
	s_ashr_i32 s3, s3, 4
	s_add_i32 s18, s3, s6
	s_mul_i32 s3, s18, 0x60
	s_sub_i32 s21, s2, s3
	s_cmp_gt_i32 s21, 63
	s_mov_b64 s[22:23], -1
	s_cbranch_scc0 .LBB0_1803
	s_ashr_i32 s19, s18, 31
	s_lshl_b64 s[2:3], s[18:19], 21
	s_add_u32 s2, s54, s2
	s_addc_u32 s3, s55, s3
	s_lshl_b32 s6, s21, 4
	s_add_i32 s6, s6, 0x7ffffc00
	s_and_b32 s24, s6, 0x7fffffc0
	s_lshl_b64 s[6:7], s[18:19], 20
	s_add_u32 s6, s77, s6
	s_addc_u32 s7, s78, s7
	s_mov_b64 s[22:23], 0

; DI ConvItem conv_item(int it, const float* wg, const float* wu, const float* wdn, bf16_t* we, bf16_t* wd) {
;     ConvItem c; const int e = it / 96; int r = it % 96;
;     if (r < 64) { const int up = r >> 5; r &= 31; c.src = (up ? wu : wg) + (size_t)e * DM * DEXP; c.ld = DEXP; c.k0 = (r >> 1) * 64; c.n0 = (r & 1) * 256; c.dst = we + (size_t)e * 1024 * 1024; c.Kd = 1024; c.mode = up; }
;     else { r -= 64; c.src = wdn + (size_t)e * DEXP * DM; c.ld = DM; c.k0 = (r >> 2) * 64; c.n0 = (r & 3) * 256; c.dst = wd + (size_t)e * 1024 * 512; c.Kd = 512; c.mode = 2; }
; DI void conv_load(const ConvItem& c, f32x4 (&v)[8], int tid) {
; #pragma unroll
;     for (int i = 0; i < 8; ++i) { const int idx = tid + 512 * i, row = idx >> 6, c4 = idx & 63; v[i] = *(const f32x4*)(c.src + (size_t)(c.k0 + row) * c.ld + c.n0 + 4 * c4); }
.LBB0_1806:
	v_add_u32_e32 v0, s24, v157
	v_add_u32_e32 v2, s24, v163
	v_add_u32_e32 v4, s24, v177
	v_mad_i64_i32 v[0:1], s[26:27], s18, v0, 0
	v_mad_i64_i32 v[2:3], s[26:27], s18, v2, 0
	v_mad_i64_i32 v[4:5], s[26:27], s18, v4, 0
	v_add_u32_e32 v6, s24, v179
	v_lshl_add_u64 v[0:1], v[0:1], 2, s[2:3]
	v_lshl_add_u64 v[2:3], v[2:3], 2, s[2:3]
	v_lshl_add_u64 v[4:5], v[4:5], 2, s[2:3]
	v_mad_i64_i32 v[6:7], s[26:27], s18, v6, 0
	v_lshl_add_u64 v[0:1], v[0:1], 0, v[64:65]
	v_lshl_add_u64 v[2:3], v[2:3], 0, v[64:65]
	v_lshl_add_u64 v[4:5], v[4:5], 0, v[64:65]
	v_lshl_add_u64 v[6:7], v[6:7], 2, s[2:3]
	global_load_dwordx4 v[8:11], v[0:1], off offset:1024 nt
	s_nop 0
	global_load_dwordx4 v[0:3], v[2:3], off offset:1024 nt
	v_lshl_add_u64 v[6:7], v[6:7], 0, v[64:65]
	global_load_dwordx4 v[24:27], v[4:5], off offset:1024 nt
	global_load_dwordx4 v[16:19], v[6:7], off offset:1024 nt
	v_add_u32_e32 v4, s24, v181
	v_mad_i64_i32 v[4:5], s[26:27], s18, v4, 0
	v_add_u32_e32 v6, s24, v183
	v_lshl_add_u64 v[4:5], v[4:5], 2, s[2:3]
	v_mad_i64_i32 v[6:7], s[26:27], s18, v6, 0
	v_lshl_add_u64 v[4:5], v[4:5], 0, v[64:65]
	v_lshl_add_u64 v[6:7], v[6:7], 2, s[2:3]
	v_lshl_add_u64 v[6:7], v[6:7], 0, v[64:65]
	global_load_dwordx4 v[40:43], v[4:5], off offset:1024 nt
	global_load_dwordx4 v[32:35], v[6:7], off offset:1024 nt
	v_add_u32_e32 v4, s24, v185
	v_mad_i64_i32 v[4:5], s[26:27], s18, v4, 0
	v_add_u32_e32 v6, s24, v187
	v_lshl_add_u64 v[4:5], v[4:5], 2, s[2:3]
	v_mad_i64_i32 v[6:7], s[18:19], s18, v6, 0
	v_lshl_add_u64 v[4:5], v[4:5], 0, v[64:65]
	v_lshl_add_u64 v[6:7], v[6:7], 2, s[2:3]
	v_lshl_add_u64 v[6:7], v[6:7], 0, v[64:65]
	global_load_dwordx4 v[86:89], v[4:5], off offset:1024 nt
	global_load_dwordx4 v[60:63], v[6:7], off offset:1024 nt
	s_or_b32 s2, s56, 2
	s_mul_hi_i32 s3, s2, 0x2aaaaaab
	s_lshr_b32 s18, s3, 31
	s_ashr_i32 s3, s3, 4
	s_add_i32 s18, s3, s18
	s_mul_i32 s3, s18, 0x60
	s_sub_i32 s21, s2, s3
	s_cmp_gt_i32 s21, 63
	s_mov_b64 s[34:35], -1
	s_cbranch_scc0 .LBB0_1808
	s_ashr_i32 s19, s18, 31
	s_lshl_b64 s[2:3], s[18:19], 21
	s_add_u32 s30, s54, s2
	s_addc_u32 s31, s55, s3
	s_lshl_b32 s2, s21, 4
	s_add_i32 s2, s2, 0x7ffffc00
	s_and_b32 s26, s2, 0x7fffffc0
	s_lshl_b64 s[2:3], s[18:19], 20
	s_add_u32 s2, s77, s2
	s_addc_u32 s3, s78, s3
	s_mov_b64 s[34:35], 0

; #define LAS __attribute__((address_space(3)))
; DI void conv_load(const ConvItem& c, f32x4 (&v)[8], int tid) {
; #pragma unroll
;     for (int i = 0; i < 8; ++i) { const int idx = tid + 512 * i, row = idx >> 6, c4 = idx & 63; v[i] = *(const f32x4*)(c.src + (size_t)(c.k0 + row) * c.ld + c.n0 + 4 * c4); }
; }
; DI void conv_store(const ConvItem& c, const f32x4 (&v)[8], LAS float* scr, int tid) {
; #pragma unroll
;     for (int i = 0; i < 8; ++i) { const int idx = tid + 512 * i, row = idx >> 6, c4 = idx & 63; LAS float* d = scr + row * 257 + 4 * c4; d[0] = v[i].x; d[1] = v[i].y; d[2] = v[i].z; d[3] = v[i].w; }
.LBB0_1811:
	v_add_u32_e32 v4, s26, v157
	v_add_u32_e32 v6, s26, v163
	v_add_u32_e32 v20, s26, v177
	v_add_u32_e32 v22, s26, v179
	v_add_u32_e32 v36, s26, v181
	v_add_u32_e32 v38, s26, v183
	v_add_u32_e32 v82, s26, v185
	v_add_u32_e32 v84, s26, v187
	v_mad_i64_i32 v[4:5], s[58:59], s34, v4, 0
	v_mad_i64_i32 v[6:7], s[58:59], s34, v6, 0
	v_mad_i64_i32 v[20:21], s[58:59], s34, v20, 0
	v_mad_i64_i32 v[22:23], s[58:59], s34, v22, 0
	v_mad_i64_i32 v[36:37], s[58:59], s34, v36, 0
	v_mad_i64_i32 v[38:39], s[58:59], s34, v38, 0
	v_mad_i64_i32 v[82:83], s[58:59], s34, v82, 0
	v_mad_i64_i32 v[84:85], s[34:35], s34, v84, 0
	v_lshl_add_u64 v[4:5], v[4:5], 2, s[30:31]
	s_lshl_b32 s44, s19, 2
	v_lshl_add_u64 v[6:7], v[6:7], 2, s[30:31]
	v_lshl_add_u64 v[20:21], v[20:21], 2, s[30:31]
	v_lshl_add_u64 v[22:23], v[22:23], 2, s[30:31]
	v_lshl_add_u64 v[36:37], v[36:37], 2, s[30:31]
	v_lshl_add_u64 v[38:39], v[38:39], 2, s[30:31]
	v_lshl_add_u64 v[82:83], v[82:83], 2, s[30:31]
	v_lshl_add_u64 v[84:85], v[84:85], 2, s[30:31]
	v_lshl_add_u64 v[4:5], v[4:5], 0, s[44:45]
	v_lshl_add_u64 v[6:7], v[6:7], 0, s[44:45]
	v_lshl_add_u64 v[20:21], v[20:21], 0, s[44:45]
	v_lshl_add_u64 v[22:23], v[22:23], 0, s[44:45]
	v_lshl_add_u64 v[36:37], v[36:37], 0, s[44:45]
	v_lshl_add_u64 v[38:39], v[38:39], 0, s[44:45]
	v_lshl_add_u64 v[82:83], v[82:83], 0, s[44:45]
	v_lshl_add_u64 v[84:85], v[84:85], 0, s[44:45]
	v_lshl_add_u64 v[4:5], v[4:5], 0, v[64:65]
	v_lshl_add_u64 v[6:7], v[6:7], 0, v[64:65]
	v_lshl_add_u64 v[20:21], v[20:21], 0, v[64:65]
	v_lshl_add_u64 v[22:23], v[22:23], 0, v[64:65]
	v_lshl_add_u64 v[36:37], v[36:37], 0, v[64:65]
	v_lshl_add_u64 v[38:39], v[38:39], 0, v[64:65]
	v_lshl_add_u64 v[82:83], v[82:83], 0, v[64:65]
	v_lshl_add_u64 v[84:85], v[84:85], 0, v[64:65]
	global_load_dwordx4 v[12:15], v[4:5], off nt
	s_nop 0
	global_load_dwordx4 v[4:7], v[6:7], off nt
	s_nop 0
	global_load_dwordx4 v[28:31], v[20:21], off nt
	s_nop 0
	global_load_dwordx4 v[20:23], v[22:23], off nt
	s_nop 0
	global_load_dwordx4 v[44:47], v[36:37], off nt
	s_nop 0
	global_load_dwordx4 v[36:39], v[38:39], off nt
	s_nop 0
	global_load_dwordx4 v[90:93], v[82:83], off nt
	s_nop 0
	global_load_dwordx4 v[82:85], v[84:85], off nt
	s_waitcnt vmcnt(23)
	ds_write2_b32 v236, v52, v53 offset1:1
	ds_write2_b32 v236, v54, v55 offset0:2 offset1:3
	s_waitcnt vmcnt(22)
	ds_write2_b32 v237, v48, v49 offset1:1
	ds_write2_b32 v237, v50, v51 offset0:2 offset1:3
	s_waitcnt vmcnt(21)
	ds_write2_b32 v238, v94, v95 offset1:1
	ds_write2_b32 v238, v96, v97 offset0:2 offset1:3
	s_waitcnt vmcnt(20)
	ds_write2_b32 v239, v56, v57 offset1:1
	ds_write2_b32 v239, v58, v59 offset0:2 offset1:3
	s_waitcnt vmcnt(19)
	ds_write2_b32 v240, v102, v103 offset1:1
	ds_write2_b32 v240, v104, v105 offset0:2 offset1:3
	s_waitcnt vmcnt(18)
	ds_write2_b32 v241, v98, v99 offset1:1
	ds_write2_b32 v241, v100, v101 offset0:2 offset1:3
	s_waitcnt vmcnt(17)
	ds_write2_b32 v242, v110, v111 offset1:1
	ds_write2_b32 v242, v112, v113 offset0:2 offset1:3
	s_waitcnt vmcnt(16)
	ds_write2_b32 v243, v106, v107 offset1:1
	ds_write2_b32 v243, v108, v109 offset0:2 offset1:3
	s_waitcnt lgkmcnt(0)
	s_barrier
; #define LAS __attribute__((address_space(3)))
; DI unsigned pk2(float lo, float hi) { f32x2 v = {lo, hi}; return __builtin_bit_cast(unsigned, __builtin_convertvector(v, bf16v2)); }
; DI ConvItem conv_item(int it, const float* wg, const float* wu, const float* wdn, bf16_t* we, bf16_t* wd) {
;     ConvItem c; const int e = it / 96; int r = it % 96;
;     if (r < 64) { const int up = r >> 5; r &= 31; c.src = (up ? wu : wg) + (size_t)e * DM * DEXP; c.ld = DEXP; c.k0 = (r >> 1) * 64; c.n0 = (r & 1) * 256; c.dst = we + (size_t)e * 1024 * 1024; c.Kd = 1024; c.mode = up; }
;     else { r -= 64; c.src = wdn + (size_t)e * DEXP * DM; c.ld = DM; c.k0 = (r >> 2) * 64; c.n0 = (r & 3) * 256; c.dst = wd + (size_t)e * 1024 * 512; c.Kd = 512; c.mode = 2; }
;     return c;
; DI void conv_store(const ConvItem& c, const f32x4 (&v)[8], LAS float* scr, int tid) {
;     ...
; #pragma unroll
;     for (int i = 0; i < 4; ++i) { const int idx = tid + 512 * i, n = idx >> 3, cc = idx & 7; const LAS float* sp = scr + (8 * cc) * 257 + n;
;         u32x4 o; o.x = pk2(sp[0], sp[257]); o.y = pk2(sp[2 * 257], sp[3 * 257]); o.z = pk2(sp[4 * 257], sp[5 * 257]); o.w = pk2(sp[6 * 257], sp[7 * 257]);
;         const int h = c.n0 + n; const int drow = (c.mode == 2) ? h : ((h >> 7) * 256 + c.mode * 128 + (h & 127));
;         *(u32x4*)(c.dst + (size_t)drow * c.Kd + c.k0 + 8 * cc) = o; }
;     __syncthreads();
	ds_read_b32 v48, v188
	ds_read_b32 v49, v188 offset:1028
	ds_read_b32 v50, v188 offset:2056
	ds_read_b32 v51, v188 offset:3084
	ds_read_b32 v52, v188 offset:4112
	ds_read_b32 v53, v188 offset:5140
	ds_read_b32 v54, v188 offset:6168
	ds_read_b32 v55, v188 offset:7196
	s_cmp_eq_u32 s29, 2
	s_cselect_b64 vcc, -1, 0
	s_lshl_b32 s21, s29, 7
	s_waitcnt lgkmcnt(6)
	v_cvt_pk_bf16_f32 v48, v48, v49
	s_waitcnt lgkmcnt(4)
	v_cvt_pk_bf16_f32 v49, v50, v51
	s_waitcnt lgkmcnt(2)
	v_cvt_pk_bf16_f32 v50, v52, v53
	v_add_u32_e32 v52, s21, v190
	v_cndmask_b32_e32 v52, v52, v150, vcc
	v_mad_i64_i32 v[52:53], s[30:31], s20, v52, 0
	s_mov_b32 s29, s45
	v_lshl_add_u64 v[52:53], v[52:53], 1, s[4:5]
	s_lshl_b64 s[28:29], s[28:29], 1
	v_lshl_add_u64 v[52:53], v[52:53], 0, s[28:29]
	v_lshlrev_b32_e32 v164, 1, v148
	v_mov_b32_e32 v165, v65
	s_waitcnt lgkmcnt(0)
	v_cvt_pk_bf16_f32 v51, v54, v55
	v_lshl_add_u64 v[52:53], v[52:53], 0, v[164:165]
	ds_read_b32 v54, v191
	ds_read_b32 v55, v191 offset:1028
	ds_read_b32 v56, v191 offset:2056
	ds_read_b32 v57, v191 offset:3084
	ds_read_b32 v58, v191 offset:4112
	ds_read_b32 v59, v191 offset:5140
	ds_read_b32 v94, v191 offset:6168
	ds_read_b32 v95, v191 offset:7196
	global_store_dwordx4 v[52:53], v[48:51], off
	v_add_u32_e32 v52, s21, v193
	v_cndmask_b32_e32 v52, v52, v152, vcc
	v_mad_i64_i32 v[52:53], s[30:31], s20, v52, 0
	v_lshl_add_u64 v[52:53], v[52:53], 1, s[4:5]
	v_lshl_add_u64 v[52:53], v[52:53], 0, s[28:29]
	s_waitcnt lgkmcnt(6)
	v_cvt_pk_bf16_f32 v48, v54, v55
	s_waitcnt lgkmcnt(4)
	v_cvt_pk_bf16_f32 v49, v56, v57
	s_waitcnt lgkmcnt(2)
	v_cvt_pk_bf16_f32 v50, v58, v59
	s_waitcnt lgkmcnt(0)
	v_cvt_pk_bf16_f32 v51, v94, v95
	v_lshl_add_u64 v[52:53], v[52:53], 0, v[164:165]
	ds_read_b32 v54, v194
	ds_read_b32 v55, v194 offset:1028
	ds_read_b32 v56, v194 offset:2056
	ds_read_b32 v57, v194 offset:3084
	ds_read_b32 v58, v194 offset:4112
	ds_read_b32 v59, v194 offset:5140
	ds_read_b32 v94, v194 offset:6168
	ds_read_b32 v95, v194 offset:7196
	global_store_dwordx4 v[52:53], v[48:51], off
	v_add_u32_e32 v52, s21, v196
	v_cndmask_b32_e32 v52, v52, v154, vcc
	v_mad_i64_i32 v[52:53], s[30:31], s20, v52, 0
	v_lshl_add_u64 v[52:53], v[52:53], 1, s[4:5]
	v_lshl_add_u64 v[52:53], v[52:53], 0, s[28:29]
	s_waitcnt lgkmcnt(6)
	v_cvt_pk_bf16_f32 v48, v54, v55
	s_waitcnt lgkmcnt(4)
	v_cvt_pk_bf16_f32 v49, v56, v57
	s_waitcnt lgkmcnt(2)
	v_cvt_pk_bf16_f32 v50, v58, v59
	s_waitcnt lgkmcnt(0)
	v_cvt_pk_bf16_f32 v51, v94, v95
	v_lshl_add_u64 v[52:53], v[52:53], 0, v[164:165]
	ds_read_b32 v54, v197
	ds_read_b32 v55, v197 offset:1028
	ds_read_b32 v56, v197 offset:2056
	ds_read_b32 v57, v197 offset:3084
	ds_read_b32 v58, v197 offset:4112
	ds_read_b32 v59, v197 offset:5140
	ds_read_b32 v94, v197 offset:6168
	ds_read_b32 v95, v197 offset:7196
	global_store_dwordx4 v[52:53], v[48:51], off
	v_add_u32_e32 v52, s21, v199
	v_cndmask_b32_e32 v52, v52, v156, vcc
	v_mad_i64_i32 v[52:53], s[20:21], s20, v52, 0
	v_lshl_add_u64 v[52:53], v[52:53], 1, s[4:5]
	s_or_b32 s4, s56, 3
	s_mul_hi_i32 s5, s4, 0x2aaaaaab
	s_lshr_b32 s20, s5, 31
	s_ashr_i32 s5, s5, 4
	s_add_i32 s20, s5, s20
	s_mul_i32 s5, s20, 0x60
	v_lshl_add_u64 v[52:53], v[52:53], 0, s[28:29]
	s_sub_i32 s23, s4, s5
	s_waitcnt lgkmcnt(6)
	v_cvt_pk_bf16_f32 v48, v54, v55
	s_waitcnt lgkmcnt(4)
	v_cvt_pk_bf16_f32 v49, v56, v57
	s_waitcnt lgkmcnt(2)
	v_cvt_pk_bf16_f32 v50, v58, v59
	s_waitcnt lgkmcnt(0)
	v_cvt_pk_bf16_f32 v51, v94, v95
	v_lshl_add_u64 v[52:53], v[52:53], 0, v[164:165]
	s_cmp_lt_i32 s23, 64
	s_mov_b64 s[34:35], -1
	global_store_dwordx4 v[52:53], v[48:51], off
	s_barrier
	s_cbranch_scc1 .LBB0_1813
	s_ashr_i32 s21, s20, 31
	s_lshl_b64 s[4:5], s[20:21], 21
	s_add_u32 s30, s54, s4
	s_addc_u32 s31, s55, s5
	s_lshl_b32 s4, s23, 4
	s_add_i32 s4, s4, 0x7ffffc00
	s_and_b32 s28, s4, 0x7fffffc0
	s_lshl_b64 s[4:5], s[20:21], 20
	s_add_u32 s4, s77, s4
	s_addc_u32 s5, s78, s5
	s_mov_b64 s[34:35], 0

; #define LAS __attribute__((address_space(3)))
; DI unsigned pk2(float lo, float hi) { f32x2 v = {lo, hi}; return __builtin_bit_cast(unsigned, __builtin_convertvector(v, bf16v2)); }
; DI void conv_load(const ConvItem& c, f32x4 (&v)[8], int tid) {
; #pragma unroll
;     for (int i = 0; i < 8; ++i) { const int idx = tid + 512 * i, row = idx >> 6, c4 = idx & 63; v[i] = *(const f32x4*)(c.src + (size_t)(c.k0 + row) * c.ld + c.n0 + 4 * c4); }
; }
; DI void conv_store(const ConvItem& c, const f32x4 (&v)[8], LAS float* scr, int tid) {
; #pragma unroll
;     for (int i = 0; i < 8; ++i) { const int idx = tid + 512 * i, row = idx >> 6, c4 = idx & 63; LAS float* d = scr + row * 257 + 4 * c4; d[0] = v[i].x; d[1] = v[i].y; d[2] = v[i].z; d[3] = v[i].w; }
;     __syncthreads();
; #pragma unroll
;     for (int i = 0; i < 4; ++i) { const int idx = tid + 512 * i, n = idx >> 3, cc = idx & 7; const LAS float* sp = scr + (8 * cc) * 257 + n;
;         u32x4 o; o.x = pk2(sp[0], sp[257]); o.y = pk2(sp[2 * 257], sp[3 * 257]); o.z = pk2(sp[4 * 257], sp[5 * 257]); o.w = pk2(sp[6 * 257], sp[7 * 257]);
;         const int h = c.n0 + n; const int drow = (c.mode == 2) ? h : ((h >> 7) * 256 + c.mode * 128 + (h & 127));
;         *(u32x4*)(c.dst + (size_t)drow * c.Kd + c.k0 + 8 * cc) = o; }
;     __syncthreads();
.LBB0_1816:
	v_add_u32_e32 v48, s28, v157
	v_add_u32_e32 v50, s28, v163
	v_add_u32_e32 v56, s28, v177
	v_add_u32_e32 v58, s28, v179
	v_add_u32_e32 v98, s28, v181
	v_add_u32_e32 v100, s28, v183
	v_add_u32_e32 v106, s28, v185
	v_add_u32_e32 v108, s28, v187
	v_mad_i64_i32 v[48:49], s[58:59], s34, v48, 0
	v_mad_i64_i32 v[50:51], s[58:59], s34, v50, 0
	v_mad_i64_i32 v[56:57], s[58:59], s34, v56, 0
	v_mad_i64_i32 v[58:59], s[58:59], s34, v58, 0
	v_mad_i64_i32 v[98:99], s[58:59], s34, v98, 0
	v_mad_i64_i32 v[100:101], s[58:59], s34, v100, 0
	v_mad_i64_i32 v[106:107], s[58:59], s34, v106, 0
	v_mad_i64_i32 v[108:109], s[34:35], s34, v108, 0
	v_lshl_add_u64 v[48:49], v[48:49], 2, s[30:31]
	s_lshl_b32 s44, s21, 2
	v_lshl_add_u64 v[50:51], v[50:51], 2, s[30:31]
	v_lshl_add_u64 v[56:57], v[56:57], 2, s[30:31]
	v_lshl_add_u64 v[58:59], v[58:59], 2, s[30:31]
	v_lshl_add_u64 v[98:99], v[98:99], 2, s[30:31]
	v_lshl_add_u64 v[100:101], v[100:101], 2, s[30:31]
	v_lshl_add_u64 v[106:107], v[106:107], 2, s[30:31]
	v_lshl_add_u64 v[108:109], v[108:109], 2, s[30:31]
	v_lshl_add_u64 v[48:49], v[48:49], 0, s[44:45]
	v_lshl_add_u64 v[50:51], v[50:51], 0, s[44:45]
	v_lshl_add_u64 v[56:57], v[56:57], 0, s[44:45]
	v_lshl_add_u64 v[58:59], v[58:59], 0, s[44:45]
	v_lshl_add_u64 v[98:99], v[98:99], 0, s[44:45]
	v_lshl_add_u64 v[100:101], v[100:101], 0, s[44:45]
	v_lshl_add_u64 v[106:107], v[106:107], 0, s[44:45]
	v_lshl_add_u64 v[108:109], v[108:109], 0, s[44:45]
	v_lshl_add_u64 v[48:49], v[48:49], 0, v[64:65]
	v_lshl_add_u64 v[50:51], v[50:51], 0, v[64:65]
	v_lshl_add_u64 v[56:57], v[56:57], 0, v[64:65]
	v_lshl_add_u64 v[58:59], v[58:59], 0, v[64:65]
	v_lshl_add_u64 v[98:99], v[98:99], 0, v[64:65]
	v_lshl_add_u64 v[100:101], v[100:101], 0, v[64:65]
	v_lshl_add_u64 v[106:107], v[106:107], 0, v[64:65]
	v_lshl_add_u64 v[108:109], v[108:109], 0, v[64:65]
	global_load_dwordx4 v[52:55], v[48:49], off nt
	s_nop 0
	global_load_dwordx4 v[48:51], v[50:51], off nt
	s_nop 0
	global_load_dwordx4 v[94:97], v[56:57], off nt
	s_nop 0
	global_load_dwordx4 v[56:59], v[58:59], off nt
	s_nop 0
	global_load_dwordx4 v[102:105], v[98:99], off nt
	s_nop 0
	global_load_dwordx4 v[98:101], v[100:101], off nt
	s_nop 0
	global_load_dwordx4 v[110:113], v[106:107], off nt
	s_nop 0
	global_load_dwordx4 v[106:109], v[108:109], off nt
	s_waitcnt vmcnt(27)
	ds_write2_b32 v236, v8, v9 offset1:1
	ds_write2_b32 v236, v10, v11 offset0:2 offset1:3
	s_waitcnt vmcnt(26)
	ds_write2_b32 v237, v0, v1 offset1:1
	ds_write2_b32 v237, v2, v3 offset0:2 offset1:3
	s_waitcnt vmcnt(25)
	ds_write2_b32 v238, v24, v25 offset1:1
	ds_write2_b32 v238, v26, v27 offset0:2 offset1:3
	s_waitcnt vmcnt(24)
	ds_write2_b32 v239, v16, v17 offset1:1
	ds_write2_b32 v239, v18, v19 offset0:2 offset1:3
	s_waitcnt vmcnt(23)
	ds_write2_b32 v240, v40, v41 offset1:1
	ds_write2_b32 v240, v42, v43 offset0:2 offset1:3
	s_waitcnt vmcnt(22)
	ds_write2_b32 v241, v32, v33 offset1:1
	ds_write2_b32 v241, v34, v35 offset0:2 offset1:3
	s_waitcnt vmcnt(21)
	ds_write2_b32 v242, v86, v87 offset1:1
	ds_write2_b32 v242, v88, v89 offset0:2 offset1:3
	s_waitcnt vmcnt(20)
	ds_write2_b32 v243, v60, v61 offset1:1
	ds_write2_b32 v243, v62, v63 offset0:2 offset1:3
	s_waitcnt lgkmcnt(0)
	s_barrier
	ds_read_b32 v0, v188
	ds_read_b32 v1, v188 offset:1028
	ds_read_b32 v2, v188 offset:2056
	ds_read_b32 v3, v188 offset:3084
	ds_read_b32 v8, v188 offset:4112
	ds_read_b32 v9, v188 offset:5140
	ds_read_b32 v10, v188 offset:6168
	ds_read_b32 v11, v188 offset:7196
	s_cmp_eq_u32 s25, 2
	s_cselect_b64 vcc, -1, 0
	s_lshl_b32 s23, s25, 7
	s_waitcnt lgkmcnt(6)
	v_cvt_pk_bf16_f32 v0, v0, v1
	s_waitcnt lgkmcnt(4)
	v_cvt_pk_bf16_f32 v1, v2, v3
	s_waitcnt lgkmcnt(2)
	v_cvt_pk_bf16_f32 v2, v8, v9
	v_add_u32_e32 v8, s23, v201
	v_cndmask_b32_e32 v8, v8, v200, vcc
	v_mad_i64_i32 v[8:9], s[30:31], s22, v8, 0
	s_mov_b32 s25, s45
	v_lshl_add_u64 v[8:9], v[8:9], 1, s[6:7]
	s_lshl_b64 s[24:25], s[24:25], 1
	v_lshl_add_u64 v[8:9], v[8:9], 0, s[24:25]
	v_mov_b32_e32 v165, v65
	s_waitcnt lgkmcnt(0)
	v_cvt_pk_bf16_f32 v3, v10, v11
	v_lshl_add_u64 v[8:9], v[8:9], 0, v[164:165]
	ds_read_b32 v10, v191
	ds_read_b32 v11, v191 offset:1028
	ds_read_b32 v16, v191 offset:2056
	ds_read_b32 v17, v191 offset:3084
	ds_read_b32 v18, v191 offset:4112
	ds_read_b32 v19, v191 offset:5140
	ds_read_b32 v24, v191 offset:6168
	ds_read_b32 v25, v191 offset:7196
	global_store_dwordx4 v[8:9], v[0:3], off
	v_add_u32_e32 v8, s23, v207
	v_cndmask_b32_e32 v8, v8, v206, vcc
	v_mad_i64_i32 v[8:9], s[30:31], s22, v8, 0
	v_lshl_add_u64 v[8:9], v[8:9], 1, s[6:7]
	v_lshl_add_u64 v[8:9], v[8:9], 0, s[24:25]
	s_waitcnt lgkmcnt(6)
	v_cvt_pk_bf16_f32 v0, v10, v11
	s_waitcnt lgkmcnt(4)
	v_cvt_pk_bf16_f32 v1, v16, v17
	s_waitcnt lgkmcnt(2)
	v_cvt_pk_bf16_f32 v2, v18, v19
	s_waitcnt lgkmcnt(0)
	v_cvt_pk_bf16_f32 v3, v24, v25
	v_lshl_add_u64 v[8:9], v[8:9], 0, v[164:165]
	ds_read_b32 v10, v194
	ds_read_b32 v11, v194 offset:1028
	ds_read_b32 v16, v194 offset:2056
	ds_read_b32 v17, v194 offset:3084
	ds_read_b32 v18, v194 offset:4112
	ds_read_b32 v19, v194 offset:5140
	ds_read_b32 v24, v194 offset:6168
	ds_read_b32 v25, v194 offset:7196
	global_store_dwordx4 v[8:9], v[0:3], off
	v_add_u32_e32 v8, s23, v209
	v_cndmask_b32_e32 v8, v8, v208, vcc
	v_mad_i64_i32 v[8:9], s[30:31], s22, v8, 0
	v_lshl_add_u64 v[8:9], v[8:9], 1, s[6:7]
	v_lshl_add_u64 v[8:9], v[8:9], 0, s[24:25]
	s_waitcnt lgkmcnt(6)
	v_cvt_pk_bf16_f32 v0, v10, v11
	s_waitcnt lgkmcnt(4)
	v_cvt_pk_bf16_f32 v1, v16, v17
	s_waitcnt lgkmcnt(2)
	v_cvt_pk_bf16_f32 v2, v18, v19
	s_waitcnt lgkmcnt(0)
	v_cvt_pk_bf16_f32 v3, v24, v25
	v_lshl_add_u64 v[8:9], v[8:9], 0, v[164:165]
	ds_read_b32 v10, v197
	ds_read_b32 v11, v197 offset:1028
	ds_read_b32 v16, v197 offset:2056
	ds_read_b32 v17, v197 offset:3084
	ds_read_b32 v18, v197 offset:4112
	ds_read_b32 v19, v197 offset:5140
	ds_read_b32 v24, v197 offset:6168
	ds_read_b32 v25, v197 offset:7196
	global_store_dwordx4 v[8:9], v[0:3], off
	v_add_u32_e32 v8, s23, v211
	v_cndmask_b32_e32 v8, v8, v210, vcc
	v_mad_i64_i32 v[8:9], s[22:23], s22, v8, 0
	v_lshl_add_u64 v[8:9], v[8:9], 1, s[6:7]
	s_add_i32 s6, s56, 4
	s_mul_hi_i32 s7, s6, 0x2aaaaaab
	s_lshr_b32 s22, s7, 31
	s_ashr_i32 s7, s7, 4
	s_add_i32 s22, s7, s22
	s_mul_i32 s7, s22, 0x60
	v_lshl_add_u64 v[8:9], v[8:9], 0, s[24:25]
	s_sub_i32 s44, s6, s7
	s_waitcnt lgkmcnt(6)
	v_cvt_pk_bf16_f32 v0, v10, v11
	s_waitcnt lgkmcnt(4)
	v_cvt_pk_bf16_f32 v1, v16, v17
	s_waitcnt lgkmcnt(2)
	v_cvt_pk_bf16_f32 v2, v18, v19
	s_waitcnt lgkmcnt(0)
	v_cvt_pk_bf16_f32 v3, v24, v25
	v_lshl_add_u64 v[8:9], v[8:9], 0, v[164:165]
	s_cmp_lt_i32 s44, 64
	s_mov_b64 s[34:35], -1
	global_store_dwordx4 v[8:9], v[0:3], off
	s_barrier
	s_cbranch_scc1 .LBB0_1818
	s_ashr_i32 s23, s22, 31
	s_lshl_b64 s[6:7], s[22:23], 21
	s_add_u32 s30, s54, s6
	s_addc_u32 s31, s55, s7
	s_lshl_b32 s6, s44, 4
	s_add_i32 s6, s6, 0x7ffffc00
	s_and_b32 s24, s6, 0x7fffffc0
	s_lshl_b64 s[6:7], s[22:23], 20
	s_add_u32 s6, s77, s6
	s_addc_u32 s7, s78, s7
	s_mov_b64 s[34:35], 0

; #define LAS __attribute__((address_space(3)))
; DI void conv_load(const ConvItem& c, f32x4 (&v)[8], int tid) {
; #pragma unroll
;     for (int i = 0; i < 8; ++i) { const int idx = tid + 512 * i, row = idx >> 6, c4 = idx & 63; v[i] = *(const f32x4*)(c.src + (size_t)(c.k0 + row) * c.ld + c.n0 + 4 * c4); }
; }
; DI void conv_store(const ConvItem& c, const f32x4 (&v)[8], LAS float* scr, int tid) {
; #pragma unroll
;     for (int i = 0; i < 8; ++i) { const int idx = tid + 512 * i, row = idx >> 6, c4 = idx & 63; LAS float* d = scr + row * 257 + 4 * c4; d[0] = v[i].x; d[1] = v[i].y; d[2] = v[i].z; d[3] = v[i].w; }
;     __syncthreads();
.LBB0_1821:
	v_add_u32_e32 v0, s24, v157
	v_add_u32_e32 v2, s24, v163
	v_add_u32_e32 v16, s24, v177
	v_add_u32_e32 v18, s24, v179
	v_add_u32_e32 v32, s24, v181
	v_add_u32_e32 v34, s24, v183
	v_add_u32_e32 v60, s24, v185
	v_add_u32_e32 v62, s24, v187
	v_mad_i64_i32 v[0:1], s[58:59], s34, v0, 0
	v_mad_i64_i32 v[2:3], s[58:59], s34, v2, 0
	v_mad_i64_i32 v[16:17], s[58:59], s34, v16, 0
	v_mad_i64_i32 v[18:19], s[58:59], s34, v18, 0
	v_mad_i64_i32 v[32:33], s[58:59], s34, v32, 0
	v_mad_i64_i32 v[34:35], s[58:59], s34, v34, 0
	v_mad_i64_i32 v[60:61], s[58:59], s34, v60, 0
	v_mad_i64_i32 v[62:63], s[34:35], s34, v62, 0
	v_lshl_add_u64 v[0:1], v[0:1], 2, s[30:31]
	v_lshl_add_u64 v[2:3], v[2:3], 2, s[30:31]
	v_lshl_add_u64 v[16:17], v[16:17], 2, s[30:31]
	v_lshl_add_u64 v[18:19], v[18:19], 2, s[30:31]
	v_lshl_add_u64 v[32:33], v[32:33], 2, s[30:31]
	v_lshl_add_u64 v[34:35], v[34:35], 2, s[30:31]
	v_lshl_add_u64 v[60:61], v[60:61], 2, s[30:31]
	v_lshl_add_u64 v[62:63], v[62:63], 2, s[30:31]
	v_lshl_add_u64 v[0:1], v[0:1], 0, v[64:65]
	v_lshl_add_u64 v[2:3], v[2:3], 0, v[64:65]
	v_lshl_add_u64 v[16:17], v[16:17], 0, v[64:65]
	v_lshl_add_u64 v[18:19], v[18:19], 0, v[64:65]
	v_lshl_add_u64 v[32:33], v[32:33], 0, v[64:65]
	v_lshl_add_u64 v[34:35], v[34:35], 0, v[64:65]
	v_lshl_add_u64 v[60:61], v[60:61], 0, v[64:65]
	v_lshl_add_u64 v[62:63], v[62:63], 0, v[64:65]
	global_load_dwordx4 v[8:11], v[0:1], off nt
	s_nop 0
	global_load_dwordx4 v[0:3], v[2:3], off nt
	s_nop 0
	global_load_dwordx4 v[24:27], v[16:17], off nt
	s_nop 0
	global_load_dwordx4 v[16:19], v[18:19], off nt
	s_nop 0
	global_load_dwordx4 v[40:43], v[32:33], off nt
	s_nop 0
	global_load_dwordx4 v[32:35], v[34:35], off nt
	s_nop 0
	global_load_dwordx4 v[86:89], v[60:61], off nt
	s_nop 0
	global_load_dwordx4 v[60:63], v[62:63], off nt
	s_waitcnt vmcnt(31)
	ds_write2_b32 v236, v12, v13 offset1:1
	ds_write2_b32 v236, v14, v15 offset0:2 offset1:3
	s_waitcnt vmcnt(30)
	ds_write2_b32 v237, v4, v5 offset1:1
	ds_write2_b32 v237, v6, v7 offset0:2 offset1:3
	s_waitcnt vmcnt(29)
	ds_write2_b32 v238, v28, v29 offset1:1
	ds_write2_b32 v238, v30, v31 offset0:2 offset1:3
	s_waitcnt vmcnt(28)
	ds_write2_b32 v239, v20, v21 offset1:1
	ds_write2_b32 v239, v22, v23 offset0:2 offset1:3
	s_waitcnt vmcnt(27)
	ds_write2_b32 v240, v44, v45 offset1:1
	ds_write2_b32 v240, v46, v47 offset0:2 offset1:3
	s_waitcnt vmcnt(26)
	ds_write2_b32 v241, v36, v37 offset1:1
	ds_write2_b32 v241, v38, v39 offset0:2 offset1:3
	s_waitcnt vmcnt(25)
	ds_write2_b32 v242, v90, v91 offset1:1
	ds_write2_b32 v242, v92, v93 offset0:2 offset1:3
	s_waitcnt vmcnt(24)
	ds_write2_b32 v243, v82, v83 offset1:1
	ds_write2_b32 v243, v84, v85 offset0:2 offset1:3
	s_waitcnt lgkmcnt(0)
	s_barrier
; #define LAS __attribute__((address_space(3)))
; DI unsigned pk2(float lo, float hi) { f32x2 v = {lo, hi}; return __builtin_bit_cast(unsigned, __builtin_convertvector(v, bf16v2)); }
; DI ConvItem conv_item(int it, const float* wg, const float* wu, const float* wdn, bf16_t* we, bf16_t* wd) {
;     ConvItem c; const int e = it / 96; int r = it % 96;
;     if (r < 64) { const int up = r >> 5; r &= 31; c.src = (up ? wu : wg) + (size_t)e * DM * DEXP; c.ld = DEXP; c.k0 = (r >> 1) * 64; c.n0 = (r & 1) * 256; c.dst = we + (size_t)e * 1024 * 1024; c.Kd = 1024; c.mode = up; }
;     else { r -= 64; c.src = wdn + (size_t)e * DEXP * DM; c.ld = DM; c.k0 = (r >> 2) * 64; c.n0 = (r & 3) * 256; c.dst = wd + (size_t)e * 1024 * 512; c.Kd = 512; c.mode = 2; }
; DI void conv_store(const ConvItem& c, const f32x4 (&v)[8], LAS float* scr, int tid) {
; #pragma unroll
;     for (int i = 0; i < 8; ++i) { const int idx = tid + 512 * i, row = idx >> 6, c4 = idx & 63; LAS float* d = scr + row * 257 + 4 * c4; d[0] = v[i].x; d[1] = v[i].y; d[2] = v[i].z; d[3] = v[i].w; }
;     __syncthreads();
; #pragma unroll
;     for (int i = 0; i < 4; ++i) { const int idx = tid + 512 * i, n = idx >> 3, cc = idx & 7; const LAS float* sp = scr + (8 * cc) * 257 + n;
;         u32x4 o; o.x = pk2(sp[0], sp[257]); o.y = pk2(sp[2 * 257], sp[3 * 257]); o.z = pk2(sp[4 * 257], sp[5 * 257]); o.w = pk2(sp[6 * 257], sp[7 * 257]);
;         const int h = c.n0 + n; const int drow = (c.mode == 2) ? h : ((h >> 7) * 256 + c.mode * 128 + (h & 127));
;         *(u32x4*)(c.dst + (size_t)drow * c.Kd + c.k0 + 8 * cc) = o; }
;     __syncthreads();
; }
	ds_read_b32 v4, v188
	ds_read_b32 v5, v188 offset:1028
	ds_read_b32 v6, v188 offset:2056
	ds_read_b32 v7, v188 offset:3084
	ds_read_b32 v12, v188 offset:4112
	ds_read_b32 v13, v188 offset:5140
	ds_read_b32 v14, v188 offset:6168
	ds_read_b32 v15, v188 offset:7196
	s_waitcnt lgkmcnt(6)
	v_cvt_pk_bf16_f32 v4, v4, v5
	s_waitcnt lgkmcnt(4)
	v_cvt_pk_bf16_f32 v5, v6, v7
	s_waitcnt lgkmcnt(2)
	v_cvt_pk_bf16_f32 v6, v12, v13
	v_add_u32_e32 v12, s19, v150
	s_cmp_eq_u32 s27, 2
	v_lshlrev_b32_e32 v13, 1, v12
	s_cselect_b64 vcc, -1, 0
	v_and_b32_e32 v13, 0xffffff00, v13
	s_lshl_b32 s23, s27, 7
	v_add_u32_e32 v13, s23, v13
	v_or_b32_e32 v13, v13, v189
	v_cndmask_b32_e32 v12, v13, v12, vcc
	v_mad_i64_i32 v[12:13], s[30:31], s18, v12, 0
	s_mov_b32 s27, s45
	v_lshl_add_u64 v[12:13], v[12:13], 1, s[2:3]
	s_lshl_b64 s[26:27], s[26:27], 1
	v_lshl_add_u64 v[12:13], v[12:13], 0, s[26:27]
	v_mov_b32_e32 v165, v65
	s_waitcnt lgkmcnt(0)
	v_cvt_pk_bf16_f32 v7, v14, v15
	v_lshl_add_u64 v[12:13], v[12:13], 0, v[164:165]
	ds_read_b32 v14, v191
	ds_read_b32 v15, v191 offset:1028
	ds_read_b32 v20, v191 offset:2056
	ds_read_b32 v21, v191 offset:3084
	ds_read_b32 v22, v191 offset:4112
	ds_read_b32 v23, v191 offset:5140
	ds_read_b32 v28, v191 offset:6168
	ds_read_b32 v29, v191 offset:7196
	global_store_dwordx4 v[12:13], v[4:7], off
	v_add_u32_e32 v12, s19, v152
	v_lshlrev_b32_e32 v13, 1, v12
	v_and_b32_e32 v13, 0xffffff00, v13
	v_add_u32_e32 v13, s23, v13
	v_or_b32_e32 v13, v13, v192
	v_cndmask_b32_e32 v12, v13, v12, vcc
	v_mad_i64_i32 v[12:13], s[30:31], s18, v12, 0
	v_lshl_add_u64 v[12:13], v[12:13], 1, s[2:3]
	v_lshl_add_u64 v[12:13], v[12:13], 0, s[26:27]
	s_waitcnt lgkmcnt(6)
	v_cvt_pk_bf16_f32 v4, v14, v15
	s_waitcnt lgkmcnt(4)
	v_cvt_pk_bf16_f32 v5, v20, v21
	s_waitcnt lgkmcnt(2)
	v_cvt_pk_bf16_f32 v6, v22, v23
	s_waitcnt lgkmcnt(0)
	v_cvt_pk_bf16_f32 v7, v28, v29
	v_lshl_add_u64 v[12:13], v[12:13], 0, v[164:165]
	ds_read_b32 v14, v194
	ds_read_b32 v15, v194 offset:1028
	ds_read_b32 v20, v194 offset:2056
	ds_read_b32 v21, v194 offset:3084
	ds_read_b32 v22, v194 offset:4112
	ds_read_b32 v23, v194 offset:5140
	ds_read_b32 v28, v194 offset:6168
	ds_read_b32 v29, v194 offset:7196
	global_store_dwordx4 v[12:13], v[4:7], off
	v_add_u32_e32 v12, s19, v154
	v_lshlrev_b32_e32 v13, 1, v12
	v_and_b32_e32 v13, 0xffffff00, v13
	v_add_u32_e32 v13, s23, v13
	v_or_b32_e32 v13, v13, v195
	v_cndmask_b32_e32 v12, v13, v12, vcc
	v_mad_i64_i32 v[12:13], s[30:31], s18, v12, 0
	v_lshl_add_u64 v[12:13], v[12:13], 1, s[2:3]
	v_lshl_add_u64 v[12:13], v[12:13], 0, s[26:27]
	s_waitcnt lgkmcnt(6)
	v_cvt_pk_bf16_f32 v4, v14, v15
	s_waitcnt lgkmcnt(4)
	v_cvt_pk_bf16_f32 v5, v20, v21
	s_waitcnt lgkmcnt(2)
	v_cvt_pk_bf16_f32 v6, v22, v23
	s_waitcnt lgkmcnt(0)
	v_cvt_pk_bf16_f32 v7, v28, v29
	v_lshl_add_u64 v[12:13], v[12:13], 0, v[164:165]
	ds_read_b32 v14, v197
	ds_read_b32 v15, v197 offset:1028
	ds_read_b32 v20, v197 offset:2056
	ds_read_b32 v21, v197 offset:3084
	ds_read_b32 v22, v197 offset:4112
	ds_read_b32 v23, v197 offset:5140
	ds_read_b32 v28, v197 offset:6168
	ds_read_b32 v29, v197 offset:7196
	global_store_dwordx4 v[12:13], v[4:7], off
	v_add_u32_e32 v12, s19, v156
	v_lshlrev_b32_e32 v13, 1, v12
	v_and_b32_e32 v13, 0xffffff00, v13
	v_add_u32_e32 v13, s23, v13
	v_or_b32_e32 v13, v13, v198
	v_cndmask_b32_e32 v12, v13, v12, vcc
	v_mad_i64_i32 v[12:13], s[18:19], s18, v12, 0
	v_lshl_add_u64 v[12:13], v[12:13], 1, s[2:3]
	s_add_i32 s2, s56, 5
	s_mul_hi_i32 s3, s2, 0x2aaaaaab
	s_lshr_b32 s18, s3, 31
	s_ashr_i32 s3, s3, 4
	s_add_i32 s18, s3, s18
	s_mul_i32 s3, s18, 0x60
	v_lshl_add_u64 v[12:13], v[12:13], 0, s[26:27]
	s_sub_i32 s23, s2, s3
	s_waitcnt lgkmcnt(6)
	v_cvt_pk_bf16_f32 v4, v14, v15
	s_waitcnt lgkmcnt(4)
	v_cvt_pk_bf16_f32 v5, v20, v21
	s_waitcnt lgkmcnt(2)
	v_cvt_pk_bf16_f32 v6, v22, v23
	s_waitcnt lgkmcnt(0)
	v_cvt_pk_bf16_f32 v7, v28, v29
	v_lshl_add_u64 v[12:13], v[12:13], 0, v[164:165]
	s_cmp_lt_i32 s23, 64
	s_mov_b64 s[34:35], -1
	global_store_dwordx4 v[12:13], v[4:7], off
	s_barrier
	s_cbranch_scc1 .LBB0_1823
	s_ashr_i32 s19, s18, 31
	s_lshl_b64 s[2:3], s[18:19], 21
	s_add_u32 s30, s54, s2
	s_addc_u32 s31, s55, s3
	s_lshl_b32 s2, s23, 4
	s_add_i32 s2, s2, 0x7ffffc00
	s_and_b32 s26, s2, 0x7fffffc0
	s_lshl_b64 s[2:3], s[18:19], 20
	s_add_u32 s2, s77, s2
	s_addc_u32 s3, s78, s3
	s_mov_b64 s[34:35], 0

; #define LAS __attribute__((address_space(3)))
; DI void conv_load(const ConvItem& c, f32x4 (&v)[8], int tid) {
; #pragma unroll
;     for (int i = 0; i < 8; ++i) { const int idx = tid + 512 * i, row = idx >> 6, c4 = idx & 63; v[i] = *(const f32x4*)(c.src + (size_t)(c.k0 + row) * c.ld + c.n0 + 4 * c4); }
; }
; DI void conv_store(const ConvItem& c, const f32x4 (&v)[8], LAS float* scr, int tid) {
; #pragma unroll
;     for (int i = 0; i < 8; ++i) { const int idx = tid + 512 * i, row = idx >> 6, c4 = idx & 63; LAS float* d = scr + row * 257 + 4 * c4; d[0] = v[i].x; d[1] = v[i].y; d[2] = v[i].z; d[3] = v[i].w; }
;     __syncthreads();
.LBB0_1826:
	v_add_u32_e32 v4, s26, v157
	v_add_u32_e32 v6, s26, v163
	v_add_u32_e32 v20, s26, v177
	v_add_u32_e32 v22, s26, v179
	v_add_u32_e32 v36, s26, v181
	v_add_u32_e32 v38, s26, v183
	v_add_u32_e32 v82, s26, v185
	v_add_u32_e32 v84, s26, v187
	v_mad_i64_i32 v[4:5], s[58:59], s34, v4, 0
	v_mad_i64_i32 v[6:7], s[58:59], s34, v6, 0
	v_mad_i64_i32 v[20:21], s[58:59], s34, v20, 0
	v_mad_i64_i32 v[22:23], s[58:59], s34, v22, 0
	v_mad_i64_i32 v[36:37], s[58:59], s34, v36, 0
	v_mad_i64_i32 v[38:39], s[58:59], s34, v38, 0
	v_mad_i64_i32 v[82:83], s[58:59], s34, v82, 0
	v_mad_i64_i32 v[84:85], s[34:35], s34, v84, 0
	v_lshl_add_u64 v[4:5], v[4:5], 2, s[30:31]
	v_lshl_add_u64 v[6:7], v[6:7], 2, s[30:31]
	v_lshl_add_u64 v[20:21], v[20:21], 2, s[30:31]
	v_lshl_add_u64 v[22:23], v[22:23], 2, s[30:31]
	v_lshl_add_u64 v[36:37], v[36:37], 2, s[30:31]
	v_lshl_add_u64 v[38:39], v[38:39], 2, s[30:31]
	v_lshl_add_u64 v[82:83], v[82:83], 2, s[30:31]
	v_lshl_add_u64 v[84:85], v[84:85], 2, s[30:31]
	v_lshl_add_u64 v[4:5], v[4:5], 0, v[64:65]
	v_lshl_add_u64 v[6:7], v[6:7], 0, v[64:65]
	v_lshl_add_u64 v[20:21], v[20:21], 0, v[64:65]
	v_lshl_add_u64 v[22:23], v[22:23], 0, v[64:65]
	v_lshl_add_u64 v[36:37], v[36:37], 0, v[64:65]
	v_lshl_add_u64 v[38:39], v[38:39], 0, v[64:65]
	v_lshl_add_u64 v[82:83], v[82:83], 0, v[64:65]
	v_lshl_add_u64 v[84:85], v[84:85], 0, v[64:65]
	global_load_dwordx4 v[12:15], v[4:5], off offset:1024 nt
	s_nop 0
	global_load_dwordx4 v[4:7], v[6:7], off offset:1024 nt
	s_nop 0
	global_load_dwordx4 v[28:31], v[20:21], off offset:1024 nt
	s_nop 0
	global_load_dwordx4 v[20:23], v[22:23], off offset:1024 nt
	s_nop 0
	global_load_dwordx4 v[44:47], v[36:37], off offset:1024 nt
	s_nop 0
	global_load_dwordx4 v[36:39], v[38:39], off offset:1024 nt
	s_nop 0
	global_load_dwordx4 v[90:93], v[82:83], off offset:1024 nt
	s_nop 0
	global_load_dwordx4 v[82:85], v[84:85], off offset:1024 nt
	s_waitcnt vmcnt(31)
	ds_write2_b32 v236, v52, v53 offset1:1
	ds_write2_b32 v236, v54, v55 offset0:2 offset1:3
	s_waitcnt vmcnt(30)
	ds_write2_b32 v237, v48, v49 offset1:1
	ds_write2_b32 v237, v50, v51 offset0:2 offset1:3
	s_waitcnt vmcnt(29)
	ds_write2_b32 v238, v94, v95 offset1:1
	ds_write2_b32 v238, v96, v97 offset0:2 offset1:3
	s_waitcnt vmcnt(28)
	ds_write2_b32 v239, v56, v57 offset1:1
	ds_write2_b32 v239, v58, v59 offset0:2 offset1:3
	s_waitcnt vmcnt(27)
	ds_write2_b32 v240, v102, v103 offset1:1
	ds_write2_b32 v240, v104, v105 offset0:2 offset1:3
	s_waitcnt vmcnt(26)
	ds_write2_b32 v241, v98, v99 offset1:1
	ds_write2_b32 v241, v100, v101 offset0:2 offset1:3
	s_waitcnt vmcnt(25)
	ds_write2_b32 v242, v110, v111 offset1:1
	ds_write2_b32 v242, v112, v113 offset0:2 offset1:3
	s_waitcnt vmcnt(24)
	ds_write2_b32 v243, v106, v107 offset1:1
	ds_write2_b32 v243, v108, v109 offset0:2 offset1:3
	s_waitcnt lgkmcnt(0)
	s_barrier
; #define LAS __attribute__((address_space(3)))
; DI unsigned pk2(float lo, float hi) { f32x2 v = {lo, hi}; return __builtin_bit_cast(unsigned, __builtin_convertvector(v, bf16v2)); }
; DI ConvItem conv_item(int it, const float* wg, const float* wu, const float* wdn, bf16_t* we, bf16_t* wd) {
;     ConvItem c; const int e = it / 96; int r = it % 96;
;     if (r < 64) { const int up = r >> 5; r &= 31; c.src = (up ? wu : wg) + (size_t)e * DM * DEXP; c.ld = DEXP; c.k0 = (r >> 1) * 64; c.n0 = (r & 1) * 256; c.dst = we + (size_t)e * 1024 * 1024; c.Kd = 1024; c.mode = up; }
;     else { r -= 64; c.src = wdn + (size_t)e * DEXP * DM; c.ld = DM; c.k0 = (r >> 2) * 64; c.n0 = (r & 3) * 256; c.dst = wd + (size_t)e * 1024 * 512; c.Kd = 512; c.mode = 2; }
; DI void conv_store(const ConvItem& c, const f32x4 (&v)[8], LAS float* scr, int tid) {
; #pragma unroll
;     for (int i = 0; i < 8; ++i) { const int idx = tid + 512 * i, row = idx >> 6, c4 = idx & 63; LAS float* d = scr + row * 257 + 4 * c4; d[0] = v[i].x; d[1] = v[i].y; d[2] = v[i].z; d[3] = v[i].w; }
;     __syncthreads();
; #pragma unroll
;     for (int i = 0; i < 4; ++i) { const int idx = tid + 512 * i, n = idx >> 3, cc = idx & 7; const LAS float* sp = scr + (8 * cc) * 257 + n;
;         u32x4 o; o.x = pk2(sp[0], sp[257]); o.y = pk2(sp[2 * 257], sp[3 * 257]); o.z = pk2(sp[4 * 257], sp[5 * 257]); o.w = pk2(sp[6 * 257], sp[7 * 257]);
;         const int h = c.n0 + n; const int drow = (c.mode == 2) ? h : ((h >> 7) * 256 + c.mode * 128 + (h & 127));
;         *(u32x4*)(c.dst + (size_t)drow * c.Kd + c.k0 + 8 * cc) = o; }
;     __syncthreads();
; }
	ds_read_b32 v48, v188
	ds_read_b32 v49, v188 offset:1028
	ds_read_b32 v50, v188 offset:2056
	ds_read_b32 v51, v188 offset:3084
	ds_read_b32 v52, v188 offset:4112
	ds_read_b32 v53, v188 offset:5140
	ds_read_b32 v54, v188 offset:6168
	ds_read_b32 v55, v188 offset:7196
	s_waitcnt lgkmcnt(6)
	v_cvt_pk_bf16_f32 v48, v48, v49
	s_waitcnt lgkmcnt(4)
	v_cvt_pk_bf16_f32 v49, v50, v51
	s_waitcnt lgkmcnt(2)
	v_cvt_pk_bf16_f32 v50, v52, v53
	v_add_u32_e32 v52, s21, v150
	s_cmp_eq_u32 s29, 2
	v_lshlrev_b32_e32 v53, 1, v52
	s_cselect_b64 vcc, -1, 0
	v_and_b32_e32 v53, 0xffffff00, v53
	s_lshl_b32 s19, s29, 7
	v_add_u32_e32 v53, s19, v53
	v_or_b32_e32 v53, v53, v189
	v_cndmask_b32_e32 v52, v53, v52, vcc
	v_mad_i64_i32 v[52:53], s[30:31], s20, v52, 0
	s_mov_b32 s29, s45
	v_lshl_add_u64 v[52:53], v[52:53], 1, s[4:5]
	s_lshl_b64 s[28:29], s[28:29], 1
	v_lshl_add_u64 v[52:53], v[52:53], 0, s[28:29]
	v_mov_b32_e32 v165, v65
	s_waitcnt lgkmcnt(0)
	v_cvt_pk_bf16_f32 v51, v54, v55
	v_lshl_add_u64 v[52:53], v[52:53], 0, v[164:165]
	ds_read_b32 v54, v191
	ds_read_b32 v55, v191 offset:1028
	ds_read_b32 v56, v191 offset:2056
	ds_read_b32 v57, v191 offset:3084
	ds_read_b32 v58, v191 offset:4112
	ds_read_b32 v59, v191 offset:5140
	ds_read_b32 v94, v191 offset:6168
	ds_read_b32 v95, v191 offset:7196
	global_store_dwordx4 v[52:53], v[48:51], off
	v_add_u32_e32 v52, s21, v152
	v_lshlrev_b32_e32 v53, 1, v52
	v_and_b32_e32 v53, 0xffffff00, v53
	v_add_u32_e32 v53, s19, v53
	v_or_b32_e32 v53, v53, v192
	v_cndmask_b32_e32 v52, v53, v52, vcc
	v_mad_i64_i32 v[52:53], s[30:31], s20, v52, 0
	v_lshl_add_u64 v[52:53], v[52:53], 1, s[4:5]
	v_lshl_add_u64 v[52:53], v[52:53], 0, s[28:29]
	s_waitcnt lgkmcnt(6)
	v_cvt_pk_bf16_f32 v48, v54, v55
	s_waitcnt lgkmcnt(4)
	v_cvt_pk_bf16_f32 v49, v56, v57
	s_waitcnt lgkmcnt(2)
	v_cvt_pk_bf16_f32 v50, v58, v59
	s_waitcnt lgkmcnt(0)
	v_cvt_pk_bf16_f32 v51, v94, v95
	v_lshl_add_u64 v[52:53], v[52:53], 0, v[164:165]
	ds_read_b32 v54, v194
	ds_read_b32 v55, v194 offset:1028
	ds_read_b32 v56, v194 offset:2056
	ds_read_b32 v57, v194 offset:3084
	ds_read_b32 v58, v194 offset:4112
	ds_read_b32 v59, v194 offset:5140
	ds_read_b32 v94, v194 offset:6168
	ds_read_b32 v95, v194 offset:7196
	global_store_dwordx4 v[52:53], v[48:51], off
	v_add_u32_e32 v52, s21, v154
	v_lshlrev_b32_e32 v53, 1, v52
	v_and_b32_e32 v53, 0xffffff00, v53
	v_add_u32_e32 v53, s19, v53
	v_or_b32_e32 v53, v53, v195
	v_cndmask_b32_e32 v52, v53, v52, vcc
	v_mad_i64_i32 v[52:53], s[30:31], s20, v52, 0
	v_lshl_add_u64 v[52:53], v[52:53], 1, s[4:5]
	v_lshl_add_u64 v[52:53], v[52:53], 0, s[28:29]
	s_waitcnt lgkmcnt(6)
	v_cvt_pk_bf16_f32 v48, v54, v55
	s_waitcnt lgkmcnt(4)
	v_cvt_pk_bf16_f32 v49, v56, v57
	s_waitcnt lgkmcnt(2)
	v_cvt_pk_bf16_f32 v50, v58, v59
	s_waitcnt lgkmcnt(0)
	v_cvt_pk_bf16_f32 v51, v94, v95
	v_lshl_add_u64 v[52:53], v[52:53], 0, v[164:165]
	ds_read_b32 v54, v197
	ds_read_b32 v55, v197 offset:1028
	ds_read_b32 v56, v197 offset:2056
	ds_read_b32 v57, v197 offset:3084
	ds_read_b32 v58, v197 offset:4112
	ds_read_b32 v59, v197 offset:5140
	ds_read_b32 v94, v197 offset:6168
	ds_read_b32 v95, v197 offset:7196
	global_store_dwordx4 v[52:53], v[48:51], off
	v_add_u32_e32 v52, s21, v156
	v_lshlrev_b32_e32 v53, 1, v52
	v_and_b32_e32 v53, 0xffffff00, v53
	v_add_u32_e32 v53, s19, v53
	v_or_b32_e32 v53, v53, v198
	v_cndmask_b32_e32 v52, v53, v52, vcc
	v_mad_i64_i32 v[52:53], s[20:21], s20, v52, 0
	v_lshl_add_u64 v[52:53], v[52:53], 1, s[4:5]
	s_add_i32 s4, s56, 6
	s_mul_hi_i32 s5, s4, 0x2aaaaaab
	s_lshr_b32 s19, s5, 31
	s_ashr_i32 s5, s5, 4
	s_add_i32 s20, s5, s19
	s_mul_i32 s5, s20, 0x60
	v_lshl_add_u64 v[52:53], v[52:53], 0, s[28:29]
	s_sub_i32 s19, s4, s5
	s_waitcnt lgkmcnt(6)
	v_cvt_pk_bf16_f32 v48, v54, v55
	s_waitcnt lgkmcnt(4)
	v_cvt_pk_bf16_f32 v49, v56, v57
	s_waitcnt lgkmcnt(2)
	v_cvt_pk_bf16_f32 v50, v58, v59
	s_waitcnt lgkmcnt(0)
	v_cvt_pk_bf16_f32 v51, v94, v95
	v_lshl_add_u64 v[52:53], v[52:53], 0, v[164:165]
	s_cmp_lt_i32 s19, 64
	s_mov_b64 s[34:35], -1
	global_store_dwordx4 v[52:53], v[48:51], off
	s_barrier
	s_cbranch_scc1 .LBB0_1828
	s_ashr_i32 s21, s20, 31
	s_lshl_b64 s[4:5], s[20:21], 21
	s_add_u32 s30, s54, s4
	s_addc_u32 s31, s55, s5
	s_lshl_b32 s4, s19, 4
	s_add_i32 s4, s4, 0x7ffffc00
	s_and_b32 s28, s4, 0x7fffffc0
	s_lshl_b64 s[4:5], s[20:21], 20
	s_add_u32 s4, s77, s4
	s_addc_u32 s5, s78, s5
	s_mov_b64 s[34:35], 0

; #define LAS __attribute__((address_space(3)))
; DI unsigned pk2(float lo, float hi) { f32x2 v = {lo, hi}; return __builtin_bit_cast(unsigned, __builtin_convertvector(v, bf16v2)); }
; DI ConvItem conv_item(int it, const float* wg, const float* wu, const float* wdn, bf16_t* we, bf16_t* wd) {
;     ConvItem c; const int e = it / 96; int r = it % 96;
;     if (r < 64) { const int up = r >> 5; r &= 31; c.src = (up ? wu : wg) + (size_t)e * DM * DEXP; c.ld = DEXP; c.k0 = (r >> 1) * 64; c.n0 = (r & 1) * 256; c.dst = we + (size_t)e * 1024 * 1024; c.Kd = 1024; c.mode = up; }
;     else { r -= 64; c.src = wdn + (size_t)e * DEXP * DM; c.ld = DM; c.k0 = (r >> 2) * 64; c.n0 = (r & 3) * 256; c.dst = wd + (size_t)e * 1024 * 512; c.Kd = 512; c.mode = 2; }
; DI void conv_load(const ConvItem& c, f32x4 (&v)[8], int tid) {
; #pragma unroll
;     for (int i = 0; i < 8; ++i) { const int idx = tid + 512 * i, row = idx >> 6, c4 = idx & 63; v[i] = *(const f32x4*)(c.src + (size_t)(c.k0 + row) * c.ld + c.n0 + 4 * c4); }
; }
; DI void conv_store(const ConvItem& c, const f32x4 (&v)[8], LAS float* scr, int tid) {
; #pragma unroll
;     for (int i = 0; i < 8; ++i) { const int idx = tid + 512 * i, row = idx >> 6, c4 = idx & 63; LAS float* d = scr + row * 257 + 4 * c4; d[0] = v[i].x; d[1] = v[i].y; d[2] = v[i].z; d[3] = v[i].w; }
;     __syncthreads();
; #pragma unroll
;     for (int i = 0; i < 4; ++i) { const int idx = tid + 512 * i, n = idx >> 3, cc = idx & 7; const LAS float* sp = scr + (8 * cc) * 257 + n;
;         u32x4 o; o.x = pk2(sp[0], sp[257]); o.y = pk2(sp[2 * 257], sp[3 * 257]); o.z = pk2(sp[4 * 257], sp[5 * 257]); o.w = pk2(sp[6 * 257], sp[7 * 257]);
;         const int h = c.n0 + n; const int drow = (c.mode == 2) ? h : ((h >> 7) * 256 + c.mode * 128 + (h & 127));
;         *(u32x4*)(c.dst + (size_t)drow * c.Kd + c.k0 + 8 * cc) = o; }
;     __syncthreads();
; }
.LBB0_1831:
	v_add_u32_e32 v48, s28, v157
	v_add_u32_e32 v50, s28, v163
	v_add_u32_e32 v52, s28, v177
	v_mad_i64_i32 v[48:49], s[58:59], s34, v48, 0
	v_mad_i64_i32 v[50:51], s[58:59], s34, v50, 0
	v_mad_i64_i32 v[52:53], s[58:59], s34, v52, 0
	v_add_u32_e32 v54, s28, v179
	v_lshl_add_u64 v[48:49], v[48:49], 2, s[30:31]
	s_lshl_b32 s44, s21, 2
	v_lshl_add_u64 v[50:51], v[50:51], 2, s[30:31]
	v_lshl_add_u64 v[52:53], v[52:53], 2, s[30:31]
	v_mad_i64_i32 v[54:55], s[58:59], s34, v54, 0
	v_lshl_add_u64 v[48:49], v[48:49], 0, s[44:45]
	v_lshl_add_u64 v[50:51], v[50:51], 0, s[44:45]
	v_lshl_add_u64 v[52:53], v[52:53], 0, s[44:45]
	v_lshl_add_u64 v[54:55], v[54:55], 2, s[30:31]
	v_lshl_add_u64 v[48:49], v[48:49], 0, v[64:65]
	v_lshl_add_u64 v[50:51], v[50:51], 0, v[64:65]
	v_lshl_add_u64 v[52:53], v[52:53], 0, v[64:65]
	v_lshl_add_u64 v[54:55], v[54:55], 0, s[44:45]
	global_load_dwordx4 v[56:59], v[48:49], off nt
	s_nop 0
	global_load_dwordx4 v[48:51], v[50:51], off nt
	v_lshl_add_u64 v[54:55], v[54:55], 0, v[64:65]
	global_load_dwordx4 v[102:105], v[52:53], off nt
	global_load_dwordx4 v[94:97], v[54:55], off nt
	v_add_u32_e32 v52, s28, v181
	v_mad_i64_i32 v[52:53], s[58:59], s34, v52, 0
	v_add_u32_e32 v54, s28, v183
	v_lshl_add_u64 v[52:53], v[52:53], 2, s[30:31]
	v_mad_i64_i32 v[54:55], s[58:59], s34, v54, 0
	v_lshl_add_u64 v[52:53], v[52:53], 0, s[44:45]
	v_lshl_add_u64 v[54:55], v[54:55], 2, s[30:31]
	v_lshl_add_u64 v[52:53], v[52:53], 0, v[64:65]
	v_lshl_add_u64 v[54:55], v[54:55], 0, s[44:45]
	v_lshl_add_u64 v[54:55], v[54:55], 0, v[64:65]
	global_load_dwordx4 v[118:121], v[52:53], off nt
	global_load_dwordx4 v[110:113], v[54:55], off nt
	v_add_u32_e32 v52, s28, v185
	v_mad_i64_i32 v[52:53], s[58:59], s34, v52, 0
	v_add_u32_e32 v54, s28, v187
	v_lshl_add_u64 v[52:53], v[52:53], 2, s[30:31]
	v_mad_i64_i32 v[54:55], s[34:35], s34, v54, 0
	v_lshl_add_u64 v[52:53], v[52:53], 0, s[44:45]
	v_lshl_add_u64 v[54:55], v[54:55], 2, s[30:31]
	v_lshl_add_u64 v[52:53], v[52:53], 0, v[64:65]
	v_lshl_add_u64 v[54:55], v[54:55], 0, s[44:45]
	v_lshl_add_u64 v[54:55], v[54:55], 0, v[64:65]
	global_load_dwordx4 v[134:137], v[52:53], off nt
	global_load_dwordx4 v[126:129], v[54:55], off nt
	s_waitcnt vmcnt(31)
	ds_write2_b32 v236, v8, v9 offset1:1
	ds_write2_b32 v236, v10, v11 offset0:2 offset1:3
	s_waitcnt vmcnt(30)
	ds_write2_b32 v237, v0, v1 offset1:1
	ds_write2_b32 v237, v2, v3 offset0:2 offset1:3
	s_waitcnt vmcnt(29)
	ds_write2_b32 v238, v24, v25 offset1:1
	ds_write2_b32 v238, v26, v27 offset0:2 offset1:3
	s_waitcnt vmcnt(28)
	ds_write2_b32 v239, v16, v17 offset1:1
	ds_write2_b32 v239, v18, v19 offset0:2 offset1:3
	s_waitcnt vmcnt(27)
	ds_write2_b32 v240, v40, v41 offset1:1
	ds_write2_b32 v240, v42, v43 offset0:2 offset1:3
	s_waitcnt vmcnt(26)
	ds_write2_b32 v241, v32, v33 offset1:1
	ds_write2_b32 v241, v34, v35 offset0:2 offset1:3
	s_waitcnt vmcnt(25)
	ds_write2_b32 v242, v86, v87 offset1:1
	ds_write2_b32 v242, v88, v89 offset0:2 offset1:3
	s_waitcnt vmcnt(24)
	ds_write2_b32 v243, v60, v61 offset1:1
	ds_write2_b32 v243, v62, v63 offset0:2 offset1:3
	s_waitcnt lgkmcnt(0)
	s_barrier
	ds_read_b32 v0, v188
	ds_read_b32 v1, v188 offset:1028
	ds_read_b32 v2, v188 offset:2056
	ds_read_b32 v3, v188 offset:3084
	ds_read_b32 v8, v188 offset:4112
	ds_read_b32 v9, v188 offset:5140
	ds_read_b32 v10, v188 offset:6168
	ds_read_b32 v11, v188 offset:7196
	s_cmp_eq_u32 s25, 2
	s_cselect_b64 vcc, -1, 0
	s_lshl_b32 s19, s25, 7
	s_waitcnt lgkmcnt(6)
	v_cvt_pk_bf16_f32 v0, v0, v1
	s_waitcnt lgkmcnt(4)
	v_cvt_pk_bf16_f32 v1, v2, v3
	s_waitcnt lgkmcnt(2)
	v_cvt_pk_bf16_f32 v2, v8, v9
	v_add_u32_e32 v8, s19, v190
	v_cndmask_b32_e32 v8, v8, v150, vcc
	v_mad_i64_i32 v[8:9], s[30:31], s22, v8, 0
	s_mov_b32 s25, s45
	v_lshl_add_u64 v[8:9], v[8:9], 1, s[6:7]
	s_lshl_b64 s[24:25], s[24:25], 1
	v_lshl_add_u64 v[8:9], v[8:9], 0, s[24:25]
	v_mov_b32_e32 v165, v65
	s_waitcnt lgkmcnt(0)
	v_cvt_pk_bf16_f32 v3, v10, v11
	v_lshl_add_u64 v[8:9], v[8:9], 0, v[164:165]
	ds_read_b32 v10, v191
	ds_read_b32 v11, v191 offset:1028
	ds_read_b32 v16, v191 offset:2056
	ds_read_b32 v17, v191 offset:3084
	ds_read_b32 v18, v191 offset:4112
	ds_read_b32 v19, v191 offset:5140
	ds_read_b32 v24, v191 offset:6168
	ds_read_b32 v25, v191 offset:7196
	global_store_dwordx4 v[8:9], v[0:3], off
	v_add_u32_e32 v8, s19, v193
	v_cndmask_b32_e32 v8, v8, v152, vcc
	v_mad_i64_i32 v[8:9], s[30:31], s22, v8, 0
	v_lshl_add_u64 v[8:9], v[8:9], 1, s[6:7]
	v_lshl_add_u64 v[8:9], v[8:9], 0, s[24:25]
	s_waitcnt lgkmcnt(6)
	v_cvt_pk_bf16_f32 v0, v10, v11
	s_waitcnt lgkmcnt(4)
	v_cvt_pk_bf16_f32 v1, v16, v17
	s_waitcnt lgkmcnt(2)
	v_cvt_pk_bf16_f32 v2, v18, v19
	s_waitcnt lgkmcnt(0)
	v_cvt_pk_bf16_f32 v3, v24, v25
	v_lshl_add_u64 v[8:9], v[8:9], 0, v[164:165]
	ds_read_b32 v10, v194
	ds_read_b32 v11, v194 offset:1028
	ds_read_b32 v16, v194 offset:2056
	ds_read_b32 v17, v194 offset:3084
	ds_read_b32 v18, v194 offset:4112
	ds_read_b32 v19, v194 offset:5140
	ds_read_b32 v24, v194 offset:6168
	ds_read_b32 v25, v194 offset:7196
	global_store_dwordx4 v[8:9], v[0:3], off
	v_add_u32_e32 v8, s19, v196
	v_cndmask_b32_e32 v8, v8, v154, vcc
	v_mad_i64_i32 v[8:9], s[30:31], s22, v8, 0
	v_lshl_add_u64 v[8:9], v[8:9], 1, s[6:7]
	v_lshl_add_u64 v[8:9], v[8:9], 0, s[24:25]
	s_waitcnt lgkmcnt(6)
	v_cvt_pk_bf16_f32 v0, v10, v11
	s_waitcnt lgkmcnt(4)
	v_cvt_pk_bf16_f32 v1, v16, v17
	s_waitcnt lgkmcnt(2)
	v_cvt_pk_bf16_f32 v2, v18, v19
	s_waitcnt lgkmcnt(0)
	v_cvt_pk_bf16_f32 v3, v24, v25
	v_lshl_add_u64 v[8:9], v[8:9], 0, v[164:165]
	ds_read_b32 v10, v197
	ds_read_b32 v11, v197 offset:1028
	ds_read_b32 v16, v197 offset:2056
	ds_read_b32 v17, v197 offset:3084
	ds_read_b32 v18, v197 offset:4112
	ds_read_b32 v19, v197 offset:5140
	ds_read_b32 v24, v197 offset:6168
	ds_read_b32 v25, v197 offset:7196
	global_store_dwordx4 v[8:9], v[0:3], off
	v_add_u32_e32 v8, s19, v199
	v_cndmask_b32_e32 v8, v8, v156, vcc
	v_mad_i64_i32 v[8:9], s[22:23], s22, v8, 0
	v_lshl_add_u64 v[8:9], v[8:9], 1, s[6:7]
	s_add_i32 s6, s56, 7
	s_mul_hi_i32 s7, s6, 0x2aaaaaab
	s_lshr_b32 s19, s7, 31
	s_ashr_i32 s7, s7, 4
	s_add_i32 s22, s7, s19
	s_mul_i32 s7, s22, 0x60
	v_lshl_add_u64 v[8:9], v[8:9], 0, s[24:25]
	s_sub_i32 s19, s6, s7
	s_waitcnt lgkmcnt(6)
	v_cvt_pk_bf16_f32 v0, v10, v11
	s_waitcnt lgkmcnt(4)
	v_cvt_pk_bf16_f32 v1, v16, v17
	s_waitcnt lgkmcnt(2)
	v_cvt_pk_bf16_f32 v2, v18, v19
	s_waitcnt lgkmcnt(0)
	v_cvt_pk_bf16_f32 v3, v24, v25
	v_lshl_add_u64 v[8:9], v[8:9], 0, v[164:165]
	s_cmp_lt_i32 s19, 64
	s_mov_b64 s[34:35], -1
	global_store_dwordx4 v[8:9], v[0:3], off
	s_barrier
	s_cbranch_scc1 .LBB0_1833
	s_ashr_i32 s23, s22, 31
	s_lshl_b64 s[6:7], s[22:23], 21
	s_add_u32 s24, s54, s6
	s_addc_u32 s25, s55, s7
	s_lshl_b32 s6, s19, 4
	s_add_i32 s6, s6, 0x7ffffc00
	s_and_b32 s30, s6, 0x7fffffc0
	s_lshl_b64 s[6:7], s[22:23], 20
	s_add_u32 s6, s77, s6
	s_addc_u32 s7, s78, s7
	s_mov_b64 s[34:35], 0

; #define LAS __attribute__((address_space(3)))
; DI unsigned pk2(float lo, float hi) { f32x2 v = {lo, hi}; return __builtin_bit_cast(unsigned, __builtin_convertvector(v, bf16v2)); }
; DI ConvItem conv_item(int it, const float* wg, const float* wu, const float* wdn, bf16_t* we, bf16_t* wd) {
;     ConvItem c; const int e = it / 96; int r = it % 96;
;     if (r < 64) { const int up = r >> 5; r &= 31; c.src = (up ? wu : wg) + (size_t)e * DM * DEXP; c.ld = DEXP; c.k0 = (r >> 1) * 64; c.n0 = (r & 1) * 256; c.dst = we + (size_t)e * 1024 * 1024; c.Kd = 1024; c.mode = up; }
;     else { r -= 64; c.src = wdn + (size_t)e * DEXP * DM; c.ld = DM; c.k0 = (r >> 2) * 64; c.n0 = (r & 3) * 256; c.dst = wd + (size_t)e * 1024 * 512; c.Kd = 512; c.mode = 2; }
; DI void conv_load(const ConvItem& c, f32x4 (&v)[8], int tid) {
; #pragma unroll
;     for (int i = 0; i < 8; ++i) { const int idx = tid + 512 * i, row = idx >> 6, c4 = idx & 63; v[i] = *(const f32x4*)(c.src + (size_t)(c.k0 + row) * c.ld + c.n0 + 4 * c4); }
; }
; DI void conv_store(const ConvItem& c, const f32x4 (&v)[8], LAS float* scr, int tid) {
; #pragma unroll
;     for (int i = 0; i < 8; ++i) { const int idx = tid + 512 * i, row = idx >> 6, c4 = idx & 63; LAS float* d = scr + row * 257 + 4 * c4; d[0] = v[i].x; d[1] = v[i].y; d[2] = v[i].z; d[3] = v[i].w; }
;     __syncthreads();
; #pragma unroll
;     for (int i = 0; i < 4; ++i) { const int idx = tid + 512 * i, n = idx >> 3, cc = idx & 7; const LAS float* sp = scr + (8 * cc) * 257 + n;
;         u32x4 o; o.x = pk2(sp[0], sp[257]); o.y = pk2(sp[2 * 257], sp[3 * 257]); o.z = pk2(sp[4 * 257], sp[5 * 257]); o.w = pk2(sp[6 * 257], sp[7 * 257]);
;         const int h = c.n0 + n; const int drow = (c.mode == 2) ? h : ((h >> 7) * 256 + c.mode * 128 + (h & 127));
;         *(u32x4*)(c.dst + (size_t)drow * c.Kd + c.k0 + 8 * cc) = o; }
;     __syncthreads();
; }
.LBB0_1836:
	v_add_u32_e32 v0, s30, v157
	v_mad_i64_i32 v[0:1], s[58:59], s34, v0, 0
	v_add_u32_e32 v2, s30, v163
	v_lshl_add_u64 v[0:1], v[0:1], 2, s[24:25]
	s_lshl_b32 s44, s23, 2
	v_mad_i64_i32 v[2:3], s[58:59], s34, v2, 0
	v_lshl_add_u64 v[0:1], v[0:1], 0, s[44:45]
	v_lshl_add_u64 v[2:3], v[2:3], 2, s[24:25]
	v_lshl_add_u64 v[0:1], v[0:1], 0, v[64:65]
	v_lshl_add_u64 v[2:3], v[2:3], 0, s[44:45]
	v_lshl_add_u64 v[2:3], v[2:3], 0, v[64:65]
	global_load_dwordx4 v[60:63], v[0:1], off nt
	global_load_dwordx4 v[52:55], v[2:3], off nt
	v_add_u32_e32 v0, s30, v177
	v_mad_i64_i32 v[0:1], s[58:59], s34, v0, 0
	v_add_u32_e32 v2, s30, v179
	v_lshl_add_u64 v[0:1], v[0:1], 2, s[24:25]
	v_mad_i64_i32 v[2:3], s[58:59], s34, v2, 0
	v_lshl_add_u64 v[0:1], v[0:1], 0, s[44:45]
	v_lshl_add_u64 v[2:3], v[2:3], 2, s[24:25]
	v_lshl_add_u64 v[0:1], v[0:1], 0, v[64:65]
	v_lshl_add_u64 v[2:3], v[2:3], 0, s[44:45]
	v_lshl_add_u64 v[2:3], v[2:3], 0, v[64:65]
	global_load_dwordx4 v[106:109], v[0:1], off nt
	global_load_dwordx4 v[98:101], v[2:3], off nt
	v_add_u32_e32 v0, s30, v181
	v_mad_i64_i32 v[0:1], s[58:59], s34, v0, 0
	v_add_u32_e32 v2, s30, v183
	v_lshl_add_u64 v[0:1], v[0:1], 2, s[24:25]
	v_mad_i64_i32 v[2:3], s[58:59], s34, v2, 0
	v_lshl_add_u64 v[0:1], v[0:1], 0, s[44:45]
	v_lshl_add_u64 v[2:3], v[2:3], 2, s[24:25]
	v_lshl_add_u64 v[0:1], v[0:1], 0, v[64:65]
	v_lshl_add_u64 v[2:3], v[2:3], 0, s[44:45]
	v_lshl_add_u64 v[2:3], v[2:3], 0, v[64:65]
	global_load_dwordx4 v[122:125], v[0:1], off nt
	global_load_dwordx4 v[114:117], v[2:3], off nt
	v_add_u32_e32 v0, s30, v185
	v_mad_i64_i32 v[0:1], s[58:59], s34, v0, 0
	v_add_u32_e32 v2, s30, v187
	v_lshl_add_u64 v[0:1], v[0:1], 2, s[24:25]
	v_mad_i64_i32 v[2:3], s[34:35], s34, v2, 0
	v_lshl_add_u64 v[0:1], v[0:1], 0, s[44:45]
	v_lshl_add_u64 v[2:3], v[2:3], 2, s[24:25]
	v_lshl_add_u64 v[0:1], v[0:1], 0, v[64:65]
	v_lshl_add_u64 v[2:3], v[2:3], 0, s[44:45]
	v_lshl_add_u64 v[2:3], v[2:3], 0, v[64:65]
	global_load_dwordx4 v[138:141], v[0:1], off nt
	global_load_dwordx4 v[130:133], v[2:3], off nt
	s_waitcnt vmcnt(31)
	ds_write2_b32 v236, v12, v13 offset1:1
	ds_write2_b32 v236, v14, v15 offset0:2 offset1:3
	s_waitcnt vmcnt(30)
	ds_write2_b32 v237, v4, v5 offset1:1
	ds_write2_b32 v237, v6, v7 offset0:2 offset1:3
	s_waitcnt vmcnt(29)
	ds_write2_b32 v238, v28, v29 offset1:1
	ds_write2_b32 v238, v30, v31 offset0:2 offset1:3
	s_waitcnt vmcnt(28)
	ds_write2_b32 v239, v20, v21 offset1:1
	ds_write2_b32 v239, v22, v23 offset0:2 offset1:3
	s_waitcnt vmcnt(27)
	ds_write2_b32 v240, v44, v45 offset1:1
	ds_write2_b32 v240, v46, v47 offset0:2 offset1:3
	s_waitcnt vmcnt(26)
	ds_write2_b32 v241, v36, v37 offset1:1
	ds_write2_b32 v241, v38, v39 offset0:2 offset1:3
	s_waitcnt vmcnt(25)
	ds_write2_b32 v242, v90, v91 offset1:1
	ds_write2_b32 v242, v92, v93 offset0:2 offset1:3
	s_waitcnt vmcnt(24)
	ds_write2_b32 v243, v82, v83 offset1:1
	ds_write2_b32 v243, v84, v85 offset0:2 offset1:3
	s_waitcnt lgkmcnt(0)
	s_barrier
	ds_read_b32 v0, v188
	ds_read_b32 v1, v188 offset:1028
	ds_read_b32 v2, v188 offset:2056
	ds_read_b32 v3, v188 offset:3084
	ds_read_b32 v4, v188 offset:4112
	ds_read_b32 v5, v188 offset:5140
	ds_read_b32 v6, v188 offset:6168
	ds_read_b32 v7, v188 offset:7196
	s_cmp_eq_u32 s27, 2
	s_cselect_b64 vcc, -1, 0
	s_lshl_b32 s19, s27, 7
	s_waitcnt lgkmcnt(6)
	v_cvt_pk_bf16_f32 v0, v0, v1
	s_waitcnt lgkmcnt(4)
	v_cvt_pk_bf16_f32 v1, v2, v3
	s_waitcnt lgkmcnt(2)
	v_cvt_pk_bf16_f32 v2, v4, v5
	v_add_u32_e32 v4, s19, v201
	v_cndmask_b32_e32 v4, v4, v200, vcc
	v_mad_i64_i32 v[4:5], s[24:25], s18, v4, 0
	s_mov_b32 s27, s45
	v_lshl_add_u64 v[4:5], v[4:5], 1, s[2:3]
	s_lshl_b64 s[24:25], s[26:27], 1
	v_lshl_add_u64 v[4:5], v[4:5], 0, s[24:25]
	v_mov_b32_e32 v165, v65
	s_waitcnt lgkmcnt(0)
	v_cvt_pk_bf16_f32 v3, v6, v7
	v_lshl_add_u64 v[4:5], v[4:5], 0, v[164:165]
	ds_read_b32 v6, v191
	ds_read_b32 v7, v191 offset:1028
	ds_read_b32 v8, v191 offset:2056
	ds_read_b32 v9, v191 offset:3084
	ds_read_b32 v10, v191 offset:4112
	ds_read_b32 v11, v191 offset:5140
	ds_read_b32 v12, v191 offset:6168
	ds_read_b32 v13, v191 offset:7196
	global_store_dwordx4 v[4:5], v[0:3], off
	v_add_u32_e32 v4, s19, v207
	v_cndmask_b32_e32 v4, v4, v206, vcc
	v_mad_i64_i32 v[4:5], s[26:27], s18, v4, 0
	v_lshl_add_u64 v[4:5], v[4:5], 1, s[2:3]
	v_lshl_add_u64 v[4:5], v[4:5], 0, s[24:25]
	s_waitcnt lgkmcnt(6)
	v_cvt_pk_bf16_f32 v0, v6, v7
	s_waitcnt lgkmcnt(4)
	v_cvt_pk_bf16_f32 v1, v8, v9
	s_waitcnt lgkmcnt(2)
	v_cvt_pk_bf16_f32 v2, v10, v11
	s_waitcnt lgkmcnt(0)
	v_cvt_pk_bf16_f32 v3, v12, v13
	v_lshl_add_u64 v[4:5], v[4:5], 0, v[164:165]
	ds_read_b32 v6, v194
	ds_read_b32 v7, v194 offset:1028
	ds_read_b32 v8, v194 offset:2056
	ds_read_b32 v9, v194 offset:3084
	ds_read_b32 v10, v194 offset:4112
	ds_read_b32 v11, v194 offset:5140
	ds_read_b32 v12, v194 offset:6168
	ds_read_b32 v13, v194 offset:7196
	global_store_dwordx4 v[4:5], v[0:3], off
	v_add_u32_e32 v4, s19, v209
	v_cndmask_b32_e32 v4, v4, v208, vcc
	v_mad_i64_i32 v[4:5], s[26:27], s18, v4, 0
	v_lshl_add_u64 v[4:5], v[4:5], 1, s[2:3]
	v_lshl_add_u64 v[4:5], v[4:5], 0, s[24:25]
	s_waitcnt lgkmcnt(6)
	v_cvt_pk_bf16_f32 v0, v6, v7
	s_waitcnt lgkmcnt(4)
	v_cvt_pk_bf16_f32 v1, v8, v9
	s_waitcnt lgkmcnt(2)
	v_cvt_pk_bf16_f32 v2, v10, v11
	s_waitcnt lgkmcnt(0)
	v_cvt_pk_bf16_f32 v3, v12, v13
	v_lshl_add_u64 v[4:5], v[4:5], 0, v[164:165]
	ds_read_b32 v6, v197
	ds_read_b32 v7, v197 offset:1028
	ds_read_b32 v8, v197 offset:2056
	ds_read_b32 v9, v197 offset:3084
	ds_read_b32 v10, v197 offset:4112
	ds_read_b32 v11, v197 offset:5140
	ds_read_b32 v12, v197 offset:6168
	ds_read_b32 v13, v197 offset:7196
	global_store_dwordx4 v[4:5], v[0:3], off
	v_add_u32_e32 v4, s19, v211
	v_cndmask_b32_e32 v4, v4, v210, vcc
	v_mad_i64_i32 v[4:5], s[18:19], s18, v4, 0
	v_lshl_add_u64 v[4:5], v[4:5], 1, s[2:3]
	s_add_i32 s2, s56, 8
	s_mul_hi_i32 s3, s2, 0x2aaaaaab
	s_lshr_b32 s18, s3, 31
	s_ashr_i32 s3, s3, 4
	s_add_i32 s18, s3, s18
	s_mul_i32 s3, s18, 0x60
	v_lshl_add_u64 v[4:5], v[4:5], 0, s[24:25]
	s_sub_i32 s44, s2, s3
	s_waitcnt lgkmcnt(6)
	v_cvt_pk_bf16_f32 v0, v6, v7
	s_waitcnt lgkmcnt(4)
	v_cvt_pk_bf16_f32 v1, v8, v9
	s_waitcnt lgkmcnt(2)
	v_cvt_pk_bf16_f32 v2, v10, v11
	s_waitcnt lgkmcnt(0)
	v_cvt_pk_bf16_f32 v3, v12, v13
	v_lshl_add_u64 v[4:5], v[4:5], 0, v[164:165]
	s_cmp_lt_i32 s44, 64
	s_mov_b64 s[34:35], -1
	global_store_dwordx4 v[4:5], v[0:3], off
	s_barrier
	s_cbranch_scc1 .LBB0_1838
	s_ashr_i32 s19, s18, 31
	s_lshl_b64 s[2:3], s[18:19], 21
	s_add_u32 s26, s54, s2
	s_addc_u32 s27, s55, s3
	s_lshl_b32 s2, s44, 4
	s_add_i32 s2, s2, 0x7ffffc00
	s_and_b32 s24, s2, 0x7fffffc0
	s_lshl_b64 s[2:3], s[18:19], 20
	s_add_u32 s2, s77, s2
	s_addc_u32 s3, s78, s3
	s_mov_b64 s[34:35], 0

; #define LAS __attribute__((address_space(3)))
; DI unsigned pk2(float lo, float hi) { f32x2 v = {lo, hi}; return __builtin_bit_cast(unsigned, __builtin_convertvector(v, bf16v2)); }
; DI ConvItem conv_item(int it, const float* wg, const float* wu, const float* wdn, bf16_t* we, bf16_t* wd) {
;     ConvItem c; const int e = it / 96; int r = it % 96;
;     if (r < 64) { const int up = r >> 5; r &= 31; c.src = (up ? wu : wg) + (size_t)e * DM * DEXP; c.ld = DEXP; c.k0 = (r >> 1) * 64; c.n0 = (r & 1) * 256; c.dst = we + (size_t)e * 1024 * 1024; c.Kd = 1024; c.mode = up; }
;     else { r -= 64; c.src = wdn + (size_t)e * DEXP * DM; c.ld = DM; c.k0 = (r >> 2) * 64; c.n0 = (r & 3) * 256; c.dst = wd + (size_t)e * 1024 * 512; c.Kd = 512; c.mode = 2; }
; DI void conv_load(const ConvItem& c, f32x4 (&v)[8], int tid) {
; #pragma unroll
;     for (int i = 0; i < 8; ++i) { const int idx = tid + 512 * i, row = idx >> 6, c4 = idx & 63; v[i] = *(const f32x4*)(c.src + (size_t)(c.k0 + row) * c.ld + c.n0 + 4 * c4); }
; }
; DI void conv_store(const ConvItem& c, const f32x4 (&v)[8], LAS float* scr, int tid) {
; #pragma unroll
;     for (int i = 0; i < 8; ++i) { const int idx = tid + 512 * i, row = idx >> 6, c4 = idx & 63; LAS float* d = scr + row * 257 + 4 * c4; d[0] = v[i].x; d[1] = v[i].y; d[2] = v[i].z; d[3] = v[i].w; }
;     __syncthreads();
; #pragma unroll
;     for (int i = 0; i < 4; ++i) { const int idx = tid + 512 * i, n = idx >> 3, cc = idx & 7; const LAS float* sp = scr + (8 * cc) * 257 + n;
;         u32x4 o; o.x = pk2(sp[0], sp[257]); o.y = pk2(sp[2 * 257], sp[3 * 257]); o.z = pk2(sp[4 * 257], sp[5 * 257]); o.w = pk2(sp[6 * 257], sp[7 * 257]);
;         const int h = c.n0 + n; const int drow = (c.mode == 2) ? h : ((h >> 7) * 256 + c.mode * 128 + (h & 127));
;         *(u32x4*)(c.dst + (size_t)drow * c.Kd + c.k0 + 8 * cc) = o; }
;     __syncthreads();
; }
.LBB0_1841:
	v_add_u32_e32 v0, s24, v157
	v_add_u32_e32 v2, s24, v163
	v_add_u32_e32 v8, s24, v177
	v_mad_i64_i32 v[0:1], s[58:59], s34, v0, 0
	v_mad_i64_i32 v[2:3], s[58:59], s34, v2, 0
	v_mad_i64_i32 v[8:9], s[58:59], s34, v8, 0
	v_add_u32_e32 v10, s24, v179
	v_lshl_add_u64 v[0:1], v[0:1], 2, s[26:27]
	v_lshl_add_u64 v[2:3], v[2:3], 2, s[26:27]
	v_lshl_add_u64 v[8:9], v[8:9], 2, s[26:27]
	v_mad_i64_i32 v[10:11], s[58:59], s34, v10, 0
	v_lshl_add_u64 v[0:1], v[0:1], 0, v[64:65]
	v_lshl_add_u64 v[2:3], v[2:3], 0, v[64:65]
	v_lshl_add_u64 v[8:9], v[8:9], 0, v[64:65]
	v_lshl_add_u64 v[10:11], v[10:11], 2, s[26:27]
	global_load_dwordx4 v[4:7], v[0:1], off nt
	s_nop 0
	global_load_dwordx4 v[0:3], v[2:3], off nt
	v_lshl_add_u64 v[10:11], v[10:11], 0, v[64:65]
	global_load_dwordx4 v[20:23], v[8:9], off nt
	global_load_dwordx4 v[16:19], v[10:11], off nt
	v_add_u32_e32 v8, s24, v181
	v_mad_i64_i32 v[8:9], s[58:59], s34, v8, 0
	v_add_u32_e32 v10, s24, v183
	v_lshl_add_u64 v[8:9], v[8:9], 2, s[26:27]
	v_mad_i64_i32 v[10:11], s[58:59], s34, v10, 0
	v_lshl_add_u64 v[8:9], v[8:9], 0, v[64:65]
	v_lshl_add_u64 v[10:11], v[10:11], 2, s[26:27]
	v_lshl_add_u64 v[10:11], v[10:11], 0, v[64:65]
	global_load_dwordx4 v[36:39], v[8:9], off nt
	global_load_dwordx4 v[32:35], v[10:11], off nt
	v_add_u32_e32 v8, s24, v185
	v_mad_i64_i32 v[8:9], s[58:59], s34, v8, 0
	v_add_u32_e32 v10, s24, v187
	v_lshl_add_u64 v[8:9], v[8:9], 2, s[26:27]
	v_mad_i64_i32 v[10:11], s[34:35], s34, v10, 0
	v_lshl_add_u64 v[8:9], v[8:9], 0, v[64:65]
	v_lshl_add_u64 v[10:11], v[10:11], 2, s[26:27]
	v_lshl_add_u64 v[10:11], v[10:11], 0, v[64:65]
	global_load_dwordx4 v[86:89], v[8:9], off nt
	global_load_dwordx4 v[82:85], v[10:11], off nt
	s_waitcnt vmcnt(31)
	ds_write2_b32 v236, v56, v57 offset1:1
	ds_write2_b32 v236, v58, v59 offset0:2 offset1:3
	s_waitcnt vmcnt(30)
	ds_write2_b32 v237, v48, v49 offset1:1
	ds_write2_b32 v237, v50, v51 offset0:2 offset1:3
	s_waitcnt vmcnt(29)
	ds_write2_b32 v238, v102, v103 offset1:1
	ds_write2_b32 v238, v104, v105 offset0:2 offset1:3
	s_waitcnt vmcnt(28)
	ds_write2_b32 v239, v94, v95 offset1:1
	ds_write2_b32 v239, v96, v97 offset0:2 offset1:3
	s_waitcnt vmcnt(27)
	ds_write2_b32 v240, v118, v119 offset1:1
	ds_write2_b32 v240, v120, v121 offset0:2 offset1:3
	s_waitcnt vmcnt(26)
	ds_write2_b32 v241, v110, v111 offset1:1
	ds_write2_b32 v241, v112, v113 offset0:2 offset1:3
	s_waitcnt vmcnt(25)
	ds_write2_b32 v242, v134, v135 offset1:1
	ds_write2_b32 v242, v136, v137 offset0:2 offset1:3
	s_waitcnt vmcnt(24)
	ds_write2_b32 v243, v126, v127 offset1:1
	ds_write2_b32 v243, v128, v129 offset0:2 offset1:3
	s_waitcnt lgkmcnt(0)
	s_barrier
	ds_read_b32 v8, v188
	ds_read_b32 v9, v188 offset:1028
	ds_read_b32 v10, v188 offset:2056
	ds_read_b32 v11, v188 offset:3084
	ds_read_b32 v12, v188 offset:4112
	ds_read_b32 v13, v188 offset:5140
	ds_read_b32 v14, v188 offset:6168
	ds_read_b32 v15, v188 offset:7196
	s_waitcnt lgkmcnt(6)
	v_cvt_pk_bf16_f32 v8, v8, v9
	s_waitcnt lgkmcnt(4)
	v_cvt_pk_bf16_f32 v9, v10, v11
	s_waitcnt lgkmcnt(2)
	v_cvt_pk_bf16_f32 v10, v12, v13
	v_add_u32_e32 v12, s21, v150
	s_cmp_eq_u32 s29, 2
	v_lshlrev_b32_e32 v13, 1, v12
	s_cselect_b64 vcc, -1, 0
	v_and_b32_e32 v13, 0xffffff00, v13
	s_lshl_b32 s19, s29, 7
	v_add_u32_e32 v13, s19, v13
	v_or_b32_e32 v13, v13, v189
	v_cndmask_b32_e32 v12, v13, v12, vcc
	v_mad_i64_i32 v[12:13], s[26:27], s20, v12, 0
	s_mov_b32 s29, s45
	v_lshl_add_u64 v[12:13], v[12:13], 1, s[4:5]
	s_lshl_b64 s[26:27], s[28:29], 1
	v_lshl_add_u64 v[12:13], v[12:13], 0, s[26:27]
	v_mov_b32_e32 v165, v65
	s_waitcnt lgkmcnt(0)
	v_cvt_pk_bf16_f32 v11, v14, v15
	v_lshl_add_u64 v[12:13], v[12:13], 0, v[164:165]
	ds_read_b32 v14, v191
	ds_read_b32 v15, v191 offset:1028
	ds_read_b32 v24, v191 offset:2056
	ds_read_b32 v25, v191 offset:3084
	ds_read_b32 v26, v191 offset:4112
	ds_read_b32 v27, v191 offset:5140
	ds_read_b32 v28, v191 offset:6168
	ds_read_b32 v29, v191 offset:7196
	global_store_dwordx4 v[12:13], v[8:11], off
	v_add_u32_e32 v12, s21, v152
	v_lshlrev_b32_e32 v13, 1, v12
	v_and_b32_e32 v13, 0xffffff00, v13
	v_add_u32_e32 v13, s19, v13
	v_or_b32_e32 v13, v13, v192
	v_cndmask_b32_e32 v12, v13, v12, vcc
	v_mad_i64_i32 v[12:13], s[28:29], s20, v12, 0
	v_lshl_add_u64 v[12:13], v[12:13], 1, s[4:5]
	v_lshl_add_u64 v[12:13], v[12:13], 0, s[26:27]
	s_waitcnt lgkmcnt(6)
	v_cvt_pk_bf16_f32 v8, v14, v15
	s_waitcnt lgkmcnt(4)
	v_cvt_pk_bf16_f32 v9, v24, v25
	s_waitcnt lgkmcnt(2)
	v_cvt_pk_bf16_f32 v10, v26, v27
	s_waitcnt lgkmcnt(0)
	v_cvt_pk_bf16_f32 v11, v28, v29
	v_lshl_add_u64 v[12:13], v[12:13], 0, v[164:165]
	ds_read_b32 v14, v194
	ds_read_b32 v15, v194 offset:1028
	ds_read_b32 v24, v194 offset:2056
	ds_read_b32 v25, v194 offset:3084
	ds_read_b32 v26, v194 offset:4112
	ds_read_b32 v27, v194 offset:5140
	ds_read_b32 v28, v194 offset:6168
	ds_read_b32 v29, v194 offset:7196
	global_store_dwordx4 v[12:13], v[8:11], off
	v_add_u32_e32 v12, s21, v154
	v_lshlrev_b32_e32 v13, 1, v12
	v_and_b32_e32 v13, 0xffffff00, v13
	v_add_u32_e32 v13, s19, v13
	v_or_b32_e32 v13, v13, v195
	v_cndmask_b32_e32 v12, v13, v12, vcc
	v_mad_i64_i32 v[12:13], s[28:29], s20, v12, 0
	v_lshl_add_u64 v[12:13], v[12:13], 1, s[4:5]
	v_lshl_add_u64 v[12:13], v[12:13], 0, s[26:27]
	s_waitcnt lgkmcnt(6)
	v_cvt_pk_bf16_f32 v8, v14, v15
	s_waitcnt lgkmcnt(4)
	v_cvt_pk_bf16_f32 v9, v24, v25
	s_waitcnt lgkmcnt(2)
	v_cvt_pk_bf16_f32 v10, v26, v27
	s_waitcnt lgkmcnt(0)
	v_cvt_pk_bf16_f32 v11, v28, v29
	v_lshl_add_u64 v[12:13], v[12:13], 0, v[164:165]
	ds_read_b32 v14, v197
	ds_read_b32 v15, v197 offset:1028
	ds_read_b32 v24, v197 offset:2056
	ds_read_b32 v25, v197 offset:3084
	ds_read_b32 v26, v197 offset:4112
	ds_read_b32 v27, v197 offset:5140
	ds_read_b32 v28, v197 offset:6168
	ds_read_b32 v29, v197 offset:7196
	global_store_dwordx4 v[12:13], v[8:11], off
	v_add_u32_e32 v12, s21, v156
	v_lshlrev_b32_e32 v13, 1, v12
	v_and_b32_e32 v13, 0xffffff00, v13
	v_add_u32_e32 v13, s19, v13
	v_or_b32_e32 v13, v13, v198
	v_cndmask_b32_e32 v12, v13, v12, vcc
	v_mad_i64_i32 v[12:13], s[20:21], s20, v12, 0
	v_lshl_add_u64 v[12:13], v[12:13], 1, s[4:5]
	s_add_i32 s4, s56, 9
	s_mul_hi_i32 s5, s4, 0x2aaaaaab
	s_lshr_b32 s19, s5, 31
	s_ashr_i32 s5, s5, 4
	s_add_i32 s20, s5, s19
	s_mul_i32 s5, s20, 0x60
	v_lshl_add_u64 v[12:13], v[12:13], 0, s[26:27]
	s_sub_i32 s19, s4, s5
	s_waitcnt lgkmcnt(6)
	v_cvt_pk_bf16_f32 v8, v14, v15
	s_waitcnt lgkmcnt(4)
	v_cvt_pk_bf16_f32 v9, v24, v25
	s_waitcnt lgkmcnt(2)
	v_cvt_pk_bf16_f32 v10, v26, v27
	s_waitcnt lgkmcnt(0)
	v_cvt_pk_bf16_f32 v11, v28, v29
	v_lshl_add_u64 v[12:13], v[12:13], 0, v[164:165]
	s_cmp_lt_i32 s19, 64
	s_mov_b64 s[34:35], -1
	global_store_dwordx4 v[12:13], v[8:11], off
	s_barrier
	s_cbranch_scc1 .LBB0_1843
	s_ashr_i32 s21, s20, 31
	s_lshl_b64 s[4:5], s[20:21], 21
	s_add_u32 s28, s54, s4
	s_addc_u32 s29, s55, s5
	s_lshl_b32 s4, s19, 4
	s_add_i32 s4, s4, 0x7ffffc00
	s_and_b32 s26, s4, 0x7fffffc0
	s_lshl_b64 s[4:5], s[20:21], 20
	s_add_u32 s4, s77, s4
	s_addc_u32 s5, s78, s5
	s_mov_b64 s[34:35], 0

; #define LAS __attribute__((address_space(3)))
; DI void conv_load(const ConvItem& c, f32x4 (&v)[8], int tid) {
; #pragma unroll
;     for (int i = 0; i < 8; ++i) { const int idx = tid + 512 * i, row = idx >> 6, c4 = idx & 63; v[i] = *(const f32x4*)(c.src + (size_t)(c.k0 + row) * c.ld + c.n0 + 4 * c4); }
; }
; DI void conv_store(const ConvItem& c, const f32x4 (&v)[8], LAS float* scr, int tid) {
; #pragma unroll
;     for (int i = 0; i < 8; ++i) { const int idx = tid + 512 * i, row = idx >> 6, c4 = idx & 63; LAS float* d = scr + row * 257 + 4 * c4; d[0] = v[i].x; d[1] = v[i].y; d[2] = v[i].z; d[3] = v[i].w; }
;     __syncthreads();
.LBB0_1846:
	v_add_u32_e32 v8, s26, v157
	v_add_u32_e32 v10, s26, v163
	v_add_u32_e32 v24, s26, v177
	v_add_u32_e32 v26, s26, v179
	v_add_u32_e32 v40, s26, v181
	v_add_u32_e32 v42, s26, v183
	v_add_u32_e32 v48, s26, v185
	v_add_u32_e32 v50, s26, v187
	v_mad_i64_i32 v[8:9], s[58:59], s34, v8, 0
	v_mad_i64_i32 v[10:11], s[58:59], s34, v10, 0
	v_mad_i64_i32 v[24:25], s[58:59], s34, v24, 0
	v_mad_i64_i32 v[26:27], s[58:59], s34, v26, 0
	v_mad_i64_i32 v[40:41], s[58:59], s34, v40, 0
	v_mad_i64_i32 v[42:43], s[58:59], s34, v42, 0
	v_mad_i64_i32 v[48:49], s[58:59], s34, v48, 0
	v_mad_i64_i32 v[50:51], s[34:35], s34, v50, 0
	v_lshl_add_u64 v[8:9], v[8:9], 2, s[28:29]
	v_lshl_add_u64 v[10:11], v[10:11], 2, s[28:29]
	v_lshl_add_u64 v[24:25], v[24:25], 2, s[28:29]
	v_lshl_add_u64 v[26:27], v[26:27], 2, s[28:29]
	v_lshl_add_u64 v[40:41], v[40:41], 2, s[28:29]
	v_lshl_add_u64 v[42:43], v[42:43], 2, s[28:29]
	v_lshl_add_u64 v[48:49], v[48:49], 2, s[28:29]
	v_lshl_add_u64 v[50:51], v[50:51], 2, s[28:29]
	v_lshl_add_u64 v[8:9], v[8:9], 0, v[64:65]
	v_lshl_add_u64 v[10:11], v[10:11], 0, v[64:65]
	v_lshl_add_u64 v[24:25], v[24:25], 0, v[64:65]
	v_lshl_add_u64 v[26:27], v[26:27], 0, v[64:65]
	v_lshl_add_u64 v[40:41], v[40:41], 0, v[64:65]
	v_lshl_add_u64 v[42:43], v[42:43], 0, v[64:65]
	v_lshl_add_u64 v[48:49], v[48:49], 0, v[64:65]
	v_lshl_add_u64 v[50:51], v[50:51], 0, v[64:65]
	global_load_dwordx4 v[12:15], v[8:9], off offset:1024 nt
	s_nop 0
	global_load_dwordx4 v[8:11], v[10:11], off offset:1024 nt
	s_nop 0
	global_load_dwordx4 v[28:31], v[24:25], off offset:1024 nt
	s_nop 0
	global_load_dwordx4 v[24:27], v[26:27], off offset:1024 nt
	s_nop 0
	global_load_dwordx4 v[44:47], v[40:41], off offset:1024 nt
	s_nop 0
	global_load_dwordx4 v[40:43], v[42:43], off offset:1024 nt
	s_nop 0
	global_load_dwordx4 v[56:59], v[48:49], off offset:1024 nt
	s_nop 0
	global_load_dwordx4 v[48:51], v[50:51], off offset:1024 nt
	s_waitcnt vmcnt(31)
	ds_write2_b32 v236, v60, v61 offset1:1
	ds_write2_b32 v236, v62, v63 offset0:2 offset1:3
	s_waitcnt vmcnt(30)
	ds_write2_b32 v237, v52, v53 offset1:1
	ds_write2_b32 v237, v54, v55 offset0:2 offset1:3
	s_waitcnt vmcnt(29)
	ds_write2_b32 v238, v106, v107 offset1:1
	ds_write2_b32 v238, v108, v109 offset0:2 offset1:3
	s_waitcnt vmcnt(28)
	ds_write2_b32 v239, v98, v99 offset1:1
	ds_write2_b32 v239, v100, v101 offset0:2 offset1:3
	s_waitcnt vmcnt(27)
	ds_write2_b32 v240, v122, v123 offset1:1
	ds_write2_b32 v240, v124, v125 offset0:2 offset1:3
	s_waitcnt vmcnt(26)
	ds_write2_b32 v241, v114, v115 offset1:1
	ds_write2_b32 v241, v116, v117 offset0:2 offset1:3
	s_waitcnt vmcnt(25)
	ds_write2_b32 v242, v138, v139 offset1:1
	ds_write2_b32 v242, v140, v141 offset0:2 offset1:3
	s_waitcnt vmcnt(24)
	ds_write2_b32 v243, v130, v131 offset1:1
	ds_write2_b32 v243, v132, v133 offset0:2 offset1:3
	s_waitcnt lgkmcnt(0)
	s_barrier
; #define LAS __attribute__((address_space(3)))
; DI unsigned pk2(float lo, float hi) { f32x2 v = {lo, hi}; return __builtin_bit_cast(unsigned, __builtin_convertvector(v, bf16v2)); }
; DI ConvItem conv_item(int it, const float* wg, const float* wu, const float* wdn, bf16_t* we, bf16_t* wd) {
;     ConvItem c; const int e = it / 96; int r = it % 96;
;     if (r < 64) { const int up = r >> 5; r &= 31; c.src = (up ? wu : wg) + (size_t)e * DM * DEXP; c.ld = DEXP; c.k0 = (r >> 1) * 64; c.n0 = (r & 1) * 256; c.dst = we + (size_t)e * 1024 * 1024; c.Kd = 1024; c.mode = up; }
;     else { r -= 64; c.src = wdn + (size_t)e * DEXP * DM; c.ld = DM; c.k0 = (r >> 2) * 64; c.n0 = (r & 3) * 256; c.dst = wd + (size_t)e * 1024 * 512; c.Kd = 512; c.mode = 2; }
; DI void conv_store(const ConvItem& c, const f32x4 (&v)[8], LAS float* scr, int tid) {
; #pragma unroll
;     for (int i = 0; i < 8; ++i) { const int idx = tid + 512 * i, row = idx >> 6, c4 = idx & 63; LAS float* d = scr + row * 257 + 4 * c4; d[0] = v[i].x; d[1] = v[i].y; d[2] = v[i].z; d[3] = v[i].w; }
;     __syncthreads();
; #pragma unroll
;     for (int i = 0; i < 4; ++i) { const int idx = tid + 512 * i, n = idx >> 3, cc = idx & 7; const LAS float* sp = scr + (8 * cc) * 257 + n;
;         u32x4 o; o.x = pk2(sp[0], sp[257]); o.y = pk2(sp[2 * 257], sp[3 * 257]); o.z = pk2(sp[4 * 257], sp[5 * 257]); o.w = pk2(sp[6 * 257], sp[7 * 257]);
;         const int h = c.n0 + n; const int drow = (c.mode == 2) ? h : ((h >> 7) * 256 + c.mode * 128 + (h & 127));
;         *(u32x4*)(c.dst + (size_t)drow * c.Kd + c.k0 + 8 * cc) = o; }
;     __syncthreads();
; }
	ds_read_b32 v52, v188
	ds_read_b32 v53, v188 offset:1028
	ds_read_b32 v54, v188 offset:2056
	ds_read_b32 v55, v188 offset:3084
	ds_read_b32 v60, v188 offset:4112
	ds_read_b32 v61, v188 offset:5140
	ds_read_b32 v62, v188 offset:6168
	ds_read_b32 v63, v188 offset:7196
	s_waitcnt lgkmcnt(6)
	v_cvt_pk_bf16_f32 v52, v52, v53
	s_waitcnt lgkmcnt(4)
	v_cvt_pk_bf16_f32 v53, v54, v55
	s_waitcnt lgkmcnt(2)
	v_cvt_pk_bf16_f32 v54, v60, v61
	v_add_u32_e32 v60, s23, v150
	s_cmp_eq_u32 s31, 2
	v_lshlrev_b32_e32 v61, 1, v60
	s_cselect_b64 vcc, -1, 0
	v_and_b32_e32 v61, 0xffffff00, v61
	s_lshl_b32 s19, s31, 7
	v_add_u32_e32 v61, s19, v61
	v_or_b32_e32 v61, v61, v189
	v_cndmask_b32_e32 v60, v61, v60, vcc
	v_mad_i64_i32 v[60:61], s[28:29], s22, v60, 0
	s_mov_b32 s31, s45
	v_lshl_add_u64 v[60:61], v[60:61], 1, s[6:7]
	s_lshl_b64 s[28:29], s[30:31], 1
	v_lshl_add_u64 v[60:61], v[60:61], 0, s[28:29]
	v_mov_b32_e32 v165, v65
	s_waitcnt lgkmcnt(0)
	v_cvt_pk_bf16_f32 v55, v62, v63
	v_lshl_add_u64 v[60:61], v[60:61], 0, v[164:165]
	ds_read_b32 v62, v191
	ds_read_b32 v63, v191 offset:1028
	ds_read_b32 v90, v191 offset:2056
	ds_read_b32 v91, v191 offset:3084
	ds_read_b32 v92, v191 offset:4112
	ds_read_b32 v93, v191 offset:5140
	ds_read_b32 v94, v191 offset:6168
	ds_read_b32 v95, v191 offset:7196
	global_store_dwordx4 v[60:61], v[52:55], off
	v_add_u32_e32 v60, s23, v152
	v_lshlrev_b32_e32 v61, 1, v60
	v_and_b32_e32 v61, 0xffffff00, v61
	v_add_u32_e32 v61, s19, v61
	v_or_b32_e32 v61, v61, v192
	v_cndmask_b32_e32 v60, v61, v60, vcc
	v_mad_i64_i32 v[60:61], s[30:31], s22, v60, 0
	v_lshl_add_u64 v[60:61], v[60:61], 1, s[6:7]
	v_lshl_add_u64 v[60:61], v[60:61], 0, s[28:29]
	s_waitcnt lgkmcnt(6)
	v_cvt_pk_bf16_f32 v52, v62, v63
	s_waitcnt lgkmcnt(4)
	v_cvt_pk_bf16_f32 v53, v90, v91
	s_waitcnt lgkmcnt(2)
	v_cvt_pk_bf16_f32 v54, v92, v93
	s_waitcnt lgkmcnt(0)
	v_cvt_pk_bf16_f32 v55, v94, v95
	v_lshl_add_u64 v[60:61], v[60:61], 0, v[164:165]
	ds_read_b32 v62, v194
	ds_read_b32 v63, v194 offset:1028
	ds_read_b32 v90, v194 offset:2056
	ds_read_b32 v91, v194 offset:3084
	ds_read_b32 v92, v194 offset:4112
	ds_read_b32 v93, v194 offset:5140
	ds_read_b32 v94, v194 offset:6168
	ds_read_b32 v95, v194 offset:7196
	global_store_dwordx4 v[60:61], v[52:55], off
	v_add_u32_e32 v60, s23, v154
	v_lshlrev_b32_e32 v61, 1, v60
	v_and_b32_e32 v61, 0xffffff00, v61
	v_add_u32_e32 v61, s19, v61
	v_or_b32_e32 v61, v61, v195
	v_cndmask_b32_e32 v60, v61, v60, vcc
	v_mad_i64_i32 v[60:61], s[30:31], s22, v60, 0
	v_lshl_add_u64 v[60:61], v[60:61], 1, s[6:7]
	v_lshl_add_u64 v[60:61], v[60:61], 0, s[28:29]
	s_waitcnt lgkmcnt(6)
	v_cvt_pk_bf16_f32 v52, v62, v63
	s_waitcnt lgkmcnt(4)
	v_cvt_pk_bf16_f32 v53, v90, v91
	s_waitcnt lgkmcnt(2)
	v_cvt_pk_bf16_f32 v54, v92, v93
	s_waitcnt lgkmcnt(0)
	v_cvt_pk_bf16_f32 v55, v94, v95
	v_lshl_add_u64 v[60:61], v[60:61], 0, v[164:165]
	ds_read_b32 v62, v197
	ds_read_b32 v63, v197 offset:1028
	ds_read_b32 v90, v197 offset:2056
	ds_read_b32 v91, v197 offset:3084
	ds_read_b32 v92, v197 offset:4112
	ds_read_b32 v93, v197 offset:5140
	ds_read_b32 v94, v197 offset:6168
	ds_read_b32 v95, v197 offset:7196
	global_store_dwordx4 v[60:61], v[52:55], off
	v_add_u32_e32 v60, s23, v156
	v_lshlrev_b32_e32 v61, 1, v60
	v_and_b32_e32 v61, 0xffffff00, v61
	v_add_u32_e32 v61, s19, v61
	v_or_b32_e32 v61, v61, v198
	v_cndmask_b32_e32 v60, v61, v60, vcc
	v_mad_i64_i32 v[60:61], s[22:23], s22, v60, 0
	v_lshl_add_u64 v[60:61], v[60:61], 1, s[6:7]
	s_add_i32 s6, s56, 10
	s_mul_hi_i32 s7, s6, 0x2aaaaaab
	s_lshr_b32 s19, s7, 31
	s_ashr_i32 s7, s7, 4
	s_add_i32 s22, s7, s19
	s_mul_i32 s7, s22, 0x60
	v_lshl_add_u64 v[60:61], v[60:61], 0, s[28:29]
	s_sub_i32 s19, s6, s7
	s_waitcnt lgkmcnt(6)
	v_cvt_pk_bf16_f32 v52, v62, v63
	s_waitcnt lgkmcnt(4)
	v_cvt_pk_bf16_f32 v53, v90, v91
	s_waitcnt lgkmcnt(2)
	v_cvt_pk_bf16_f32 v54, v92, v93
	s_waitcnt lgkmcnt(0)
	v_cvt_pk_bf16_f32 v55, v94, v95
	v_lshl_add_u64 v[60:61], v[60:61], 0, v[164:165]
	s_cmp_lt_i32 s19, 64
	s_mov_b64 s[34:35], -1
	global_store_dwordx4 v[60:61], v[52:55], off
	s_barrier
	s_cbranch_scc1 .LBB0_1848
	s_ashr_i32 s23, s22, 31
	s_lshl_b64 s[6:7], s[22:23], 21
	s_add_u32 s30, s54, s6
	s_addc_u32 s31, s55, s7
	s_lshl_b32 s6, s19, 4
	s_add_i32 s6, s6, 0x7ffffc00
	s_and_b32 s28, s6, 0x7fffffc0
	s_lshl_b64 s[6:7], s[22:23], 20
	s_add_u32 s6, s77, s6
	s_addc_u32 s7, s78, s7
	s_mov_b64 s[34:35], 0

; #define LAS __attribute__((address_space(3)))
; DI unsigned pk2(float lo, float hi) { f32x2 v = {lo, hi}; return __builtin_bit_cast(unsigned, __builtin_convertvector(v, bf16v2)); }
; DI ConvItem conv_item(int it, const float* wg, const float* wu, const float* wdn, bf16_t* we, bf16_t* wd) {
;     ConvItem c; const int e = it / 96; int r = it % 96;
;     if (r < 64) { const int up = r >> 5; r &= 31; c.src = (up ? wu : wg) + (size_t)e * DM * DEXP; c.ld = DEXP; c.k0 = (r >> 1) * 64; c.n0 = (r & 1) * 256; c.dst = we + (size_t)e * 1024 * 1024; c.Kd = 1024; c.mode = up; }
;     else { r -= 64; c.src = wdn + (size_t)e * DEXP * DM; c.ld = DM; c.k0 = (r >> 2) * 64; c.n0 = (r & 3) * 256; c.dst = wd + (size_t)e * 1024 * 512; c.Kd = 512; c.mode = 2; }
; DI void conv_load(const ConvItem& c, f32x4 (&v)[8], int tid) {
; #pragma unroll
;     for (int i = 0; i < 8; ++i) { const int idx = tid + 512 * i, row = idx >> 6, c4 = idx & 63; v[i] = *(const f32x4*)(c.src + (size_t)(c.k0 + row) * c.ld + c.n0 + 4 * c4); }
; }
; DI void conv_store(const ConvItem& c, const f32x4 (&v)[8], LAS float* scr, int tid) {
; #pragma unroll
;     for (int i = 0; i < 8; ++i) { const int idx = tid + 512 * i, row = idx >> 6, c4 = idx & 63; LAS float* d = scr + row * 257 + 4 * c4; d[0] = v[i].x; d[1] = v[i].y; d[2] = v[i].z; d[3] = v[i].w; }
;     __syncthreads();
; #pragma unroll
;     for (int i = 0; i < 4; ++i) { const int idx = tid + 512 * i, n = idx >> 3, cc = idx & 7; const LAS float* sp = scr + (8 * cc) * 257 + n;
;         u32x4 o; o.x = pk2(sp[0], sp[257]); o.y = pk2(sp[2 * 257], sp[3 * 257]); o.z = pk2(sp[4 * 257], sp[5 * 257]); o.w = pk2(sp[6 * 257], sp[7 * 257]);
;         const int h = c.n0 + n; const int drow = (c.mode == 2) ? h : ((h >> 7) * 256 + c.mode * 128 + (h & 127));
;         *(u32x4*)(c.dst + (size_t)drow * c.Kd + c.k0 + 8 * cc) = o; }
;     __syncthreads();
; }
.LBB0_1851:
	v_add_u32_e32 v52, s28, v157
	v_add_u32_e32 v54, s28, v163
	v_add_u32_e32 v90, s28, v177
	v_add_u32_e32 v92, s28, v179
	v_add_u32_e32 v98, s28, v181
	v_add_u32_e32 v100, s28, v183
	v_add_u32_e32 v106, s28, v185
	v_add_u32_e32 v108, s28, v187
	v_mad_i64_i32 v[52:53], s[58:59], s34, v52, 0
	v_mad_i64_i32 v[54:55], s[58:59], s34, v54, 0
	v_mad_i64_i32 v[90:91], s[58:59], s34, v90, 0
	v_mad_i64_i32 v[92:93], s[58:59], s34, v92, 0
	v_mad_i64_i32 v[98:99], s[58:59], s34, v98, 0
	v_mad_i64_i32 v[100:101], s[58:59], s34, v100, 0
	v_mad_i64_i32 v[106:107], s[58:59], s34, v106, 0
	v_mad_i64_i32 v[108:109], s[34:35], s34, v108, 0
	v_lshl_add_u64 v[52:53], v[52:53], 2, s[30:31]
	s_lshl_b32 s44, s21, 2
	v_lshl_add_u64 v[54:55], v[54:55], 2, s[30:31]
	v_lshl_add_u64 v[90:91], v[90:91], 2, s[30:31]
	v_lshl_add_u64 v[92:93], v[92:93], 2, s[30:31]
	v_lshl_add_u64 v[98:99], v[98:99], 2, s[30:31]
	v_lshl_add_u64 v[100:101], v[100:101], 2, s[30:31]
	v_lshl_add_u64 v[106:107], v[106:107], 2, s[30:31]
	v_lshl_add_u64 v[108:109], v[108:109], 2, s[30:31]
	v_lshl_add_u64 v[52:53], v[52:53], 0, s[44:45]
	v_lshl_add_u64 v[54:55], v[54:55], 0, s[44:45]
	v_lshl_add_u64 v[90:91], v[90:91], 0, s[44:45]
	v_lshl_add_u64 v[92:93], v[92:93], 0, s[44:45]
	v_lshl_add_u64 v[98:99], v[98:99], 0, s[44:45]
	v_lshl_add_u64 v[100:101], v[100:101], 0, s[44:45]
	v_lshl_add_u64 v[106:107], v[106:107], 0, s[44:45]
	v_lshl_add_u64 v[108:109], v[108:109], 0, s[44:45]
	v_lshl_add_u64 v[52:53], v[52:53], 0, v[64:65]
	v_lshl_add_u64 v[54:55], v[54:55], 0, v[64:65]
	v_lshl_add_u64 v[90:91], v[90:91], 0, v[64:65]
	v_lshl_add_u64 v[92:93], v[92:93], 0, v[64:65]
	v_lshl_add_u64 v[98:99], v[98:99], 0, v[64:65]
	v_lshl_add_u64 v[100:101], v[100:101], 0, v[64:65]
	v_lshl_add_u64 v[106:107], v[106:107], 0, v[64:65]
	v_lshl_add_u64 v[108:109], v[108:109], 0, v[64:65]
	global_load_dwordx4 v[60:63], v[52:53], off nt
	s_nop 0
	global_load_dwordx4 v[52:55], v[54:55], off nt
	s_nop 0
	global_load_dwordx4 v[94:97], v[90:91], off nt
	s_nop 0
	global_load_dwordx4 v[90:93], v[92:93], off nt
	s_nop 0
	global_load_dwordx4 v[102:105], v[98:99], off nt
	s_nop 0
	global_load_dwordx4 v[98:101], v[100:101], off nt
	s_nop 0
	global_load_dwordx4 v[110:113], v[106:107], off nt
	s_nop 0
	global_load_dwordx4 v[106:109], v[108:109], off nt
	s_waitcnt vmcnt(31)
	ds_write2_b32 v236, v4, v5 offset1:1
	ds_write2_b32 v236, v6, v7 offset0:2 offset1:3
	s_waitcnt vmcnt(30)
	ds_write2_b32 v237, v0, v1 offset1:1
	ds_write2_b32 v237, v2, v3 offset0:2 offset1:3
	s_waitcnt vmcnt(29)
	ds_write2_b32 v238, v20, v21 offset1:1
	ds_write2_b32 v238, v22, v23 offset0:2 offset1:3
	s_waitcnt vmcnt(28)
	ds_write2_b32 v239, v16, v17 offset1:1
	ds_write2_b32 v239, v18, v19 offset0:2 offset1:3
	s_waitcnt vmcnt(27)
	ds_write2_b32 v240, v36, v37 offset1:1
	ds_write2_b32 v240, v38, v39 offset0:2 offset1:3
	s_waitcnt vmcnt(26)
	ds_write2_b32 v241, v32, v33 offset1:1
	ds_write2_b32 v241, v34, v35 offset0:2 offset1:3
	s_waitcnt vmcnt(25)
	ds_write2_b32 v242, v86, v87 offset1:1
	ds_write2_b32 v242, v88, v89 offset0:2 offset1:3
	s_waitcnt vmcnt(24)
	ds_write2_b32 v243, v82, v83 offset1:1
	ds_write2_b32 v243, v84, v85 offset0:2 offset1:3
	s_waitcnt lgkmcnt(0)
	s_barrier
	ds_read_b32 v0, v188
	ds_read_b32 v1, v188 offset:1028
	ds_read_b32 v2, v188 offset:2056
	ds_read_b32 v3, v188 offset:3084
	ds_read_b32 v4, v188 offset:4112
	ds_read_b32 v5, v188 offset:5140
	ds_read_b32 v6, v188 offset:6168
	ds_read_b32 v7, v188 offset:7196
	s_cmp_eq_u32 s25, 2
	s_cselect_b64 vcc, -1, 0
	s_lshl_b32 s19, s25, 7
	s_waitcnt lgkmcnt(6)
	v_cvt_pk_bf16_f32 v0, v0, v1
	s_waitcnt lgkmcnt(4)
	v_cvt_pk_bf16_f32 v1, v2, v3
	s_waitcnt lgkmcnt(2)
	v_cvt_pk_bf16_f32 v2, v4, v5
	v_add_u32_e32 v4, s19, v190
	v_cndmask_b32_e32 v4, v4, v150, vcc
	v_mad_i64_i32 v[4:5], s[30:31], s18, v4, 0
	s_mov_b32 s25, s45
	v_lshl_add_u64 v[4:5], v[4:5], 1, s[2:3]
	s_lshl_b64 s[24:25], s[24:25], 1
	v_lshl_add_u64 v[4:5], v[4:5], 0, s[24:25]
	v_mov_b32_e32 v165, v65
	s_waitcnt lgkmcnt(0)
	v_cvt_pk_bf16_f32 v3, v6, v7
	v_lshl_add_u64 v[4:5], v[4:5], 0, v[164:165]
	ds_read_b32 v6, v191
	ds_read_b32 v7, v191 offset:1028
	ds_read_b32 v16, v191 offset:2056
	ds_read_b32 v17, v191 offset:3084
	ds_read_b32 v18, v191 offset:4112
	ds_read_b32 v19, v191 offset:5140
	ds_read_b32 v20, v191 offset:6168
	ds_read_b32 v21, v191 offset:7196
	global_store_dwordx4 v[4:5], v[0:3], off
	v_add_u32_e32 v4, s19, v193
	v_cndmask_b32_e32 v4, v4, v152, vcc
	v_mad_i64_i32 v[4:5], s[30:31], s18, v4, 0
	v_lshl_add_u64 v[4:5], v[4:5], 1, s[2:3]
	v_lshl_add_u64 v[4:5], v[4:5], 0, s[24:25]
	s_waitcnt lgkmcnt(6)
	v_cvt_pk_bf16_f32 v0, v6, v7
	s_waitcnt lgkmcnt(4)
	v_cvt_pk_bf16_f32 v1, v16, v17
	s_waitcnt lgkmcnt(2)
	v_cvt_pk_bf16_f32 v2, v18, v19
	s_waitcnt lgkmcnt(0)
	v_cvt_pk_bf16_f32 v3, v20, v21
	v_lshl_add_u64 v[4:5], v[4:5], 0, v[164:165]
	ds_read_b32 v6, v194
	ds_read_b32 v7, v194 offset:1028
	ds_read_b32 v16, v194 offset:2056
	ds_read_b32 v17, v194 offset:3084
	ds_read_b32 v18, v194 offset:4112
	ds_read_b32 v19, v194 offset:5140
	ds_read_b32 v20, v194 offset:6168
	ds_read_b32 v21, v194 offset:7196
	global_store_dwordx4 v[4:5], v[0:3], off
	v_add_u32_e32 v4, s19, v196
	v_cndmask_b32_e32 v4, v4, v154, vcc
	v_mad_i64_i32 v[4:5], s[30:31], s18, v4, 0
	v_lshl_add_u64 v[4:5], v[4:5], 1, s[2:3]
	v_lshl_add_u64 v[4:5], v[4:5], 0, s[24:25]
	s_waitcnt lgkmcnt(6)
	v_cvt_pk_bf16_f32 v0, v6, v7
	s_waitcnt lgkmcnt(4)
	v_cvt_pk_bf16_f32 v1, v16, v17
	s_waitcnt lgkmcnt(2)
	v_cvt_pk_bf16_f32 v2, v18, v19
	s_waitcnt lgkmcnt(0)
	v_cvt_pk_bf16_f32 v3, v20, v21
	v_lshl_add_u64 v[4:5], v[4:5], 0, v[164:165]
	ds_read_b32 v6, v197
	ds_read_b32 v7, v197 offset:1028
	ds_read_b32 v16, v197 offset:2056
	ds_read_b32 v17, v197 offset:3084
	ds_read_b32 v18, v197 offset:4112
	ds_read_b32 v19, v197 offset:5140
	ds_read_b32 v20, v197 offset:6168
	ds_read_b32 v21, v197 offset:7196
	global_store_dwordx4 v[4:5], v[0:3], off
	v_add_u32_e32 v4, s19, v199
	v_cndmask_b32_e32 v4, v4, v156, vcc
	v_mad_i64_i32 v[4:5], s[18:19], s18, v4, 0
	s_add_i32 s56, s56, 11
	v_lshl_add_u64 v[4:5], v[4:5], 1, s[2:3]
	s_mul_hi_i32 s2, s56, 0x2aaaaaab
	s_lshr_b32 s3, s2, 31
	s_ashr_i32 s2, s2, 4
	s_add_i32 s18, s2, s3
	s_mul_i32 s2, s18, 0x60
	v_lshl_add_u64 v[4:5], v[4:5], 0, s[24:25]
	s_sub_i32 s25, s56, s2
	s_waitcnt lgkmcnt(6)
	v_cvt_pk_bf16_f32 v0, v6, v7
	s_waitcnt lgkmcnt(4)
	v_cvt_pk_bf16_f32 v1, v16, v17
	s_waitcnt lgkmcnt(2)
	v_cvt_pk_bf16_f32 v2, v18, v19
	s_waitcnt lgkmcnt(0)
	v_cvt_pk_bf16_f32 v3, v20, v21
	v_lshl_add_u64 v[4:5], v[4:5], 0, v[164:165]
	s_cmp_lt_i32 s25, 64
	s_mov_b64 s[34:35], -1
	global_store_dwordx4 v[4:5], v[0:3], off
	s_barrier
	s_cbranch_scc1 .LBB0_1853
	s_ashr_i32 s19, s18, 31
	s_lshl_b64 s[2:3], s[18:19], 21
	s_add_u32 s30, s54, s2
	s_addc_u32 s31, s55, s3
	s_lshl_b32 s2, s25, 4
	s_add_i32 s2, s2, 0x7ffffc00
	s_and_b32 s24, s2, 0x7fffffc0
	s_lshl_b64 s[2:3], s[18:19], 20
	s_add_u32 s2, s77, s2
	s_addc_u32 s3, s78, s3
	s_mov_b64 s[34:35], 0

; #define LAS __attribute__((address_space(3)))
; DI unsigned pk2(float lo, float hi) { f32x2 v = {lo, hi}; return __builtin_bit_cast(unsigned, __builtin_convertvector(v, bf16v2)); }
; DI void conv_load(const ConvItem& c, f32x4 (&v)[8], int tid) {
; #pragma unroll
;     for (int i = 0; i < 8; ++i) { const int idx = tid + 512 * i, row = idx >> 6, c4 = idx & 63; v[i] = *(const f32x4*)(c.src + (size_t)(c.k0 + row) * c.ld + c.n0 + 4 * c4); }
; }
; DI void conv_store(const ConvItem& c, const f32x4 (&v)[8], LAS float* scr, int tid) {
; #pragma unroll
;     for (int i = 0; i < 8; ++i) { const int idx = tid + 512 * i, row = idx >> 6, c4 = idx & 63; LAS float* d = scr + row * 257 + 4 * c4; d[0] = v[i].x; d[1] = v[i].y; d[2] = v[i].z; d[3] = v[i].w; }
;     __syncthreads();
; #pragma unroll
;     for (int i = 0; i < 4; ++i) { const int idx = tid + 512 * i, n = idx >> 3, cc = idx & 7; const LAS float* sp = scr + (8 * cc) * 257 + n;
;         u32x4 o; o.x = pk2(sp[0], sp[257]); o.y = pk2(sp[2 * 257], sp[3 * 257]); o.z = pk2(sp[4 * 257], sp[5 * 257]); o.w = pk2(sp[6 * 257], sp[7 * 257]);
;         const int h = c.n0 + n; const int drow = (c.mode == 2) ? h : ((h >> 7) * 256 + c.mode * 128 + (h & 127));
;         *(u32x4*)(c.dst + (size_t)drow * c.Kd + c.k0 + 8 * cc) = o; }
;     __syncthreads();
; }
; DI void conv_experts_items(Frame& F, int l, int it_lo, int it_hi, int it_step) {
;     ...
;     c[0] = conv_item(it_lo, wg, wu, wdn, we, wd); conv_load(c[0], r[0], F.tid);
;     c[1] = conv_item(it_lo + 1, wg, wu, wdn, we, wd); conv_load(c[1], r[1], F.tid);
; #pragma unroll
;     for (int k = 0; k < CONV_GROUP; ++k) {
;         if (k + 2 < CONV_GROUP) { c[(k + 2) % 3] = conv_item(it_lo + k + 2, wg, wu, wdn, we, wd); conv_load(c[(k + 2) % 3], r[(k + 2) % 3], F.tid); }
;         conv_store(c[k % 3], r[k % 3], scr, F.tid);
;     }
.LBB0_1856:
	v_add_u32_e32 v0, s24, v157
	v_add_u32_e32 v2, s24, v163
	v_add_u32_e32 v16, s24, v177
	v_add_u32_e32 v18, s24, v179
	v_add_u32_e32 v32, s24, v181
	v_add_u32_e32 v34, s24, v183
	v_add_u32_e32 v82, s24, v185
	v_add_u32_e32 v84, s24, v187
	v_mad_i64_i32 v[0:1], s[50:51], s34, v0, 0
	v_mad_i64_i32 v[2:3], s[50:51], s34, v2, 0
	v_mad_i64_i32 v[16:17], s[50:51], s34, v16, 0
	v_mad_i64_i32 v[18:19], s[50:51], s34, v18, 0
	v_mad_i64_i32 v[32:33], s[50:51], s34, v32, 0
	v_mad_i64_i32 v[34:35], s[50:51], s34, v34, 0
	v_mad_i64_i32 v[82:83], s[50:51], s34, v82, 0
	v_mad_i64_i32 v[84:85], s[34:35], s34, v84, 0
	v_lshl_add_u64 v[0:1], v[0:1], 2, s[30:31]
	s_lshl_b32 s44, s19, 2
	v_lshl_add_u64 v[2:3], v[2:3], 2, s[30:31]
	v_lshl_add_u64 v[16:17], v[16:17], 2, s[30:31]
	v_lshl_add_u64 v[18:19], v[18:19], 2, s[30:31]
	v_lshl_add_u64 v[32:33], v[32:33], 2, s[30:31]
	v_lshl_add_u64 v[34:35], v[34:35], 2, s[30:31]
	v_lshl_add_u64 v[82:83], v[82:83], 2, s[30:31]
	v_lshl_add_u64 v[84:85], v[84:85], 2, s[30:31]
	v_lshl_add_u64 v[0:1], v[0:1], 0, s[44:45]
	v_lshl_add_u64 v[2:3], v[2:3], 0, s[44:45]
	v_lshl_add_u64 v[16:17], v[16:17], 0, s[44:45]
	v_lshl_add_u64 v[18:19], v[18:19], 0, s[44:45]
	v_lshl_add_u64 v[32:33], v[32:33], 0, s[44:45]
	v_lshl_add_u64 v[34:35], v[34:35], 0, s[44:45]
	v_lshl_add_u64 v[82:83], v[82:83], 0, s[44:45]
	v_lshl_add_u64 v[84:85], v[84:85], 0, s[44:45]
	v_lshl_add_u64 v[0:1], v[0:1], 0, v[64:65]
	v_lshl_add_u64 v[2:3], v[2:3], 0, v[64:65]
	v_lshl_add_u64 v[16:17], v[16:17], 0, v[64:65]
	v_lshl_add_u64 v[18:19], v[18:19], 0, v[64:65]
	v_lshl_add_u64 v[32:33], v[32:33], 0, v[64:65]
	v_lshl_add_u64 v[34:35], v[34:35], 0, v[64:65]
	v_lshl_add_u64 v[82:83], v[82:83], 0, v[64:65]
	v_lshl_add_u64 v[84:85], v[84:85], 0, v[64:65]
	global_load_dwordx4 v[4:7], v[0:1], off nt
	s_nop 0
	global_load_dwordx4 v[0:3], v[2:3], off nt
	s_nop 0
	global_load_dwordx4 v[20:23], v[16:17], off nt
	s_nop 0
	global_load_dwordx4 v[16:19], v[18:19], off nt
	s_nop 0
	global_load_dwordx4 v[36:39], v[32:33], off nt
	s_nop 0
	global_load_dwordx4 v[32:35], v[34:35], off nt
	s_nop 0
	global_load_dwordx4 v[86:89], v[82:83], off nt
	s_nop 0
	global_load_dwordx4 v[82:85], v[84:85], off nt
	s_waitcnt vmcnt(31)
	ds_write2_b32 v236, v12, v13 offset1:1
	ds_write2_b32 v236, v14, v15 offset0:2 offset1:3
	s_waitcnt vmcnt(30)
	ds_write2_b32 v237, v8, v9 offset1:1
	ds_write2_b32 v237, v10, v11 offset0:2 offset1:3
	s_waitcnt vmcnt(29)
	ds_write2_b32 v238, v28, v29 offset1:1
	ds_write2_b32 v238, v30, v31 offset0:2 offset1:3
	s_waitcnt vmcnt(28)
	ds_write2_b32 v239, v24, v25 offset1:1
	ds_write2_b32 v239, v26, v27 offset0:2 offset1:3
	s_waitcnt vmcnt(27)
	ds_write2_b32 v240, v44, v45 offset1:1
	ds_write2_b32 v240, v46, v47 offset0:2 offset1:3
	s_waitcnt vmcnt(26)
	ds_write2_b32 v241, v40, v41 offset1:1
	ds_write2_b32 v241, v42, v43 offset0:2 offset1:3
	s_waitcnt vmcnt(25)
	ds_write2_b32 v242, v56, v57 offset1:1
	ds_write2_b32 v242, v58, v59 offset0:2 offset1:3
	s_waitcnt vmcnt(24)
	ds_write2_b32 v243, v48, v49 offset1:1
	ds_write2_b32 v243, v50, v51 offset0:2 offset1:3
	s_waitcnt lgkmcnt(0)
	s_barrier
	ds_read_b32 v8, v188
	ds_read_b32 v9, v188 offset:1028
	ds_read_b32 v10, v188 offset:2056
	ds_read_b32 v11, v188 offset:3084
	ds_read_b32 v12, v188 offset:4112
	ds_read_b32 v13, v188 offset:5140
	ds_read_b32 v14, v188 offset:6168
	ds_read_b32 v15, v188 offset:7196
	s_cmp_eq_u32 s27, 2
	s_cselect_b64 vcc, -1, 0
	s_lshl_b32 s25, s27, 7
	s_waitcnt lgkmcnt(6)
	v_cvt_pk_bf16_f32 v8, v8, v9
	s_waitcnt lgkmcnt(4)
	v_cvt_pk_bf16_f32 v9, v10, v11
	s_waitcnt lgkmcnt(2)
	v_cvt_pk_bf16_f32 v10, v12, v13
	v_add_u32_e32 v12, s25, v201
	v_cndmask_b32_e32 v12, v12, v200, vcc
	v_mad_i64_i32 v[12:13], s[30:31], s20, v12, 0
	s_mov_b32 s27, s45
	v_lshl_add_u64 v[12:13], v[12:13], 1, s[4:5]
	s_lshl_b64 s[26:27], s[26:27], 1
	v_lshl_add_u64 v[12:13], v[12:13], 0, s[26:27]
	v_mov_b32_e32 v165, v65
	s_waitcnt lgkmcnt(0)
	v_cvt_pk_bf16_f32 v11, v14, v15
	v_lshl_add_u64 v[12:13], v[12:13], 0, v[164:165]
	ds_read_b32 v14, v191
	ds_read_b32 v15, v191 offset:1028
	ds_read_b32 v24, v191 offset:2056
	ds_read_b32 v25, v191 offset:3084
	ds_read_b32 v26, v191 offset:4112
	ds_read_b32 v27, v191 offset:5140
	ds_read_b32 v28, v191 offset:6168
	ds_read_b32 v29, v191 offset:7196
	global_store_dwordx4 v[12:13], v[8:11], off
	v_add_u32_e32 v12, s25, v207
	v_cndmask_b32_e32 v12, v12, v206, vcc
	v_mad_i64_i32 v[12:13], s[30:31], s20, v12, 0
	v_lshl_add_u64 v[12:13], v[12:13], 1, s[4:5]
	v_lshl_add_u64 v[12:13], v[12:13], 0, s[26:27]
	s_waitcnt lgkmcnt(6)
	v_cvt_pk_bf16_f32 v8, v14, v15
	s_waitcnt lgkmcnt(4)
	v_cvt_pk_bf16_f32 v9, v24, v25
	s_waitcnt lgkmcnt(2)
	v_cvt_pk_bf16_f32 v10, v26, v27
	s_waitcnt lgkmcnt(0)
	v_cvt_pk_bf16_f32 v11, v28, v29
	v_lshl_add_u64 v[12:13], v[12:13], 0, v[164:165]
	ds_read_b32 v14, v194
	ds_read_b32 v15, v194 offset:1028
	ds_read_b32 v24, v194 offset:2056
	ds_read_b32 v25, v194 offset:3084
	ds_read_b32 v26, v194 offset:4112
	ds_read_b32 v27, v194 offset:5140
	ds_read_b32 v28, v194 offset:6168
	ds_read_b32 v29, v194 offset:7196
	global_store_dwordx4 v[12:13], v[8:11], off
	v_add_u32_e32 v12, s25, v209
	v_cndmask_b32_e32 v12, v12, v208, vcc
	v_mad_i64_i32 v[12:13], s[30:31], s20, v12, 0
	v_lshl_add_u64 v[12:13], v[12:13], 1, s[4:5]
	v_lshl_add_u64 v[12:13], v[12:13], 0, s[26:27]
	s_waitcnt lgkmcnt(6)
	v_cvt_pk_bf16_f32 v8, v14, v15
	s_waitcnt lgkmcnt(4)
	v_cvt_pk_bf16_f32 v9, v24, v25
	s_waitcnt lgkmcnt(2)
	v_cvt_pk_bf16_f32 v10, v26, v27
	s_waitcnt lgkmcnt(0)
	v_cvt_pk_bf16_f32 v11, v28, v29
	v_lshl_add_u64 v[12:13], v[12:13], 0, v[164:165]
	ds_read_b32 v14, v197
	ds_read_b32 v15, v197 offset:1028
	ds_read_b32 v24, v197 offset:2056
	ds_read_b32 v25, v197 offset:3084
	ds_read_b32 v26, v197 offset:4112
	ds_read_b32 v27, v197 offset:5140
	ds_read_b32 v28, v197 offset:6168
	ds_read_b32 v29, v197 offset:7196
	global_store_dwordx4 v[12:13], v[8:11], off
	v_add_u32_e32 v12, s25, v211
	v_cndmask_b32_e32 v12, v12, v210, vcc
	v_mad_i64_i32 v[12:13], s[30:31], s20, v12, 0
	v_lshl_add_u64 v[12:13], v[12:13], 1, s[4:5]
	v_lshl_add_u64 v[12:13], v[12:13], 0, s[26:27]
	s_waitcnt lgkmcnt(6)
	v_cvt_pk_bf16_f32 v8, v14, v15
	s_waitcnt lgkmcnt(4)
	v_cvt_pk_bf16_f32 v9, v24, v25
	s_waitcnt lgkmcnt(2)
	v_cvt_pk_bf16_f32 v10, v26, v27
	s_waitcnt lgkmcnt(0)
	v_cvt_pk_bf16_f32 v11, v28, v29
	v_lshl_add_u64 v[12:13], v[12:13], 0, v[164:165]
	global_store_dwordx4 v[12:13], v[8:11], off
	s_barrier
; #define LAS __attribute__((address_space(3)))
; DI unsigned pk2(float lo, float hi) { f32x2 v = {lo, hi}; return __builtin_bit_cast(unsigned, __builtin_convertvector(v, bf16v2)); }
; DI void conv_store(const ConvItem& c, const f32x4 (&v)[8], LAS float* scr, int tid) {
; #pragma unroll
;     for (int i = 0; i < 8; ++i) { const int idx = tid + 512 * i, row = idx >> 6, c4 = idx & 63; LAS float* d = scr + row * 257 + 4 * c4; d[0] = v[i].x; d[1] = v[i].y; d[2] = v[i].z; d[3] = v[i].w; }
;     __syncthreads();
; #pragma unroll
;     for (int i = 0; i < 4; ++i) { const int idx = tid + 512 * i, n = idx >> 3, cc = idx & 7; const LAS float* sp = scr + (8 * cc) * 257 + n;
;         u32x4 o; o.x = pk2(sp[0], sp[257]); o.y = pk2(sp[2 * 257], sp[3 * 257]); o.z = pk2(sp[4 * 257], sp[5 * 257]); o.w = pk2(sp[6 * 257], sp[7 * 257]);
;         const int h = c.n0 + n; const int drow = (c.mode == 2) ? h : ((h >> 7) * 256 + c.mode * 128 + (h & 127));
;         *(u32x4*)(c.dst + (size_t)drow * c.Kd + c.k0 + 8 * cc) = o; }
;     __syncthreads();
; }
	s_waitcnt vmcnt(23)
	ds_write2_b32 v236, v60, v61 offset1:1
	ds_write2_b32 v236, v62, v63 offset0:2 offset1:3
	s_waitcnt vmcnt(22)
	ds_write2_b32 v237, v52, v53 offset1:1
	ds_write2_b32 v237, v54, v55 offset0:2 offset1:3
	s_waitcnt vmcnt(21)
	ds_write2_b32 v238, v94, v95 offset1:1
	ds_write2_b32 v238, v96, v97 offset0:2 offset1:3
	s_waitcnt vmcnt(20)
	ds_write2_b32 v239, v90, v91 offset1:1
	ds_write2_b32 v239, v92, v93 offset0:2 offset1:3
	s_waitcnt vmcnt(19)
	ds_write2_b32 v240, v102, v103 offset1:1
	ds_write2_b32 v240, v104, v105 offset0:2 offset1:3
	s_waitcnt vmcnt(18)
	ds_write2_b32 v241, v98, v99 offset1:1
	ds_write2_b32 v241, v100, v101 offset0:2 offset1:3
	s_waitcnt vmcnt(17)
	ds_write2_b32 v242, v110, v111 offset1:1
	ds_write2_b32 v242, v112, v113 offset0:2 offset1:3
	s_waitcnt vmcnt(16)
	ds_write2_b32 v243, v106, v107 offset1:1
	ds_write2_b32 v243, v108, v109 offset0:2 offset1:3
	s_waitcnt lgkmcnt(0)
	s_barrier
	ds_read_b32 v8, v188
	ds_read_b32 v9, v188 offset:1028
	ds_read_b32 v10, v188 offset:2056
	ds_read_b32 v11, v188 offset:3084
	ds_read_b32 v12, v188 offset:4112
	ds_read_b32 v13, v188 offset:5140
	ds_read_b32 v14, v188 offset:6168
	ds_read_b32 v15, v188 offset:7196
	s_waitcnt lgkmcnt(6)
	v_cvt_pk_bf16_f32 v8, v8, v9
	s_waitcnt lgkmcnt(4)
	v_cvt_pk_bf16_f32 v9, v10, v11
	s_waitcnt lgkmcnt(2)
	v_cvt_pk_bf16_f32 v10, v12, v13
	v_add_u32_e32 v12, s21, v150
	s_cmp_eq_u32 s29, 2
	v_lshlrev_b32_e32 v13, 1, v12
	s_cselect_b64 vcc, -1, 0
	v_and_b32_e32 v13, 0xffffff00, v13
	s_lshl_b32 s20, s29, 7
	v_add_u32_e32 v13, s20, v13
	v_or_b32_e32 v13, v13, v189
	v_cndmask_b32_e32 v12, v13, v12, vcc
	v_mad_i64_i32 v[12:13], s[4:5], s22, v12, 0
	s_mov_b32 s29, s45
	v_lshl_add_u64 v[12:13], v[12:13], 1, s[6:7]
	s_lshl_b64 s[4:5], s[28:29], 1
	v_lshl_add_u64 v[12:13], v[12:13], 0, s[4:5]
	s_waitcnt lgkmcnt(0)
	v_cvt_pk_bf16_f32 v11, v14, v15
	v_lshl_add_u64 v[12:13], v[12:13], 0, v[164:165]
	ds_read_b32 v14, v191
	ds_read_b32 v15, v191 offset:1028
	ds_read_b32 v24, v191 offset:2056
	ds_read_b32 v25, v191 offset:3084
	ds_read_b32 v26, v191 offset:4112
	ds_read_b32 v27, v191 offset:5140
	ds_read_b32 v28, v191 offset:6168
	ds_read_b32 v29, v191 offset:7196
	global_store_dwordx4 v[12:13], v[8:11], off
	v_add_u32_e32 v12, s21, v152
	v_lshlrev_b32_e32 v13, 1, v12
	v_and_b32_e32 v13, 0xffffff00, v13
	v_add_u32_e32 v13, s20, v13
	v_or_b32_e32 v13, v13, v192
	v_cndmask_b32_e32 v12, v13, v12, vcc
	v_mad_i64_i32 v[12:13], s[26:27], s22, v12, 0
	v_lshl_add_u64 v[12:13], v[12:13], 1, s[6:7]
	v_lshl_add_u64 v[12:13], v[12:13], 0, s[4:5]
	s_waitcnt lgkmcnt(6)
	v_cvt_pk_bf16_f32 v8, v14, v15
	s_waitcnt lgkmcnt(4)
	v_cvt_pk_bf16_f32 v9, v24, v25
	s_waitcnt lgkmcnt(2)
	v_cvt_pk_bf16_f32 v10, v26, v27
	s_waitcnt lgkmcnt(0)
	v_cvt_pk_bf16_f32 v11, v28, v29
	v_lshl_add_u64 v[12:13], v[12:13], 0, v[164:165]
	ds_read_b32 v14, v194
	ds_read_b32 v15, v194 offset:1028
	ds_read_b32 v24, v194 offset:2056
	ds_read_b32 v25, v194 offset:3084
	ds_read_b32 v26, v194 offset:4112
	ds_read_b32 v27, v194 offset:5140
	ds_read_b32 v28, v194 offset:6168
	ds_read_b32 v29, v194 offset:7196
	global_store_dwordx4 v[12:13], v[8:11], off
	v_add_u32_e32 v12, s21, v154
	v_lshlrev_b32_e32 v13, 1, v12
	v_and_b32_e32 v13, 0xffffff00, v13
	v_add_u32_e32 v13, s20, v13
	v_or_b32_e32 v13, v13, v195
	v_cndmask_b32_e32 v12, v13, v12, vcc
	v_mad_i64_i32 v[12:13], s[26:27], s22, v12, 0
	v_lshl_add_u64 v[12:13], v[12:13], 1, s[6:7]
	v_lshl_add_u64 v[12:13], v[12:13], 0, s[4:5]
	s_waitcnt lgkmcnt(6)
	v_cvt_pk_bf16_f32 v8, v14, v15
	s_waitcnt lgkmcnt(4)
	v_cvt_pk_bf16_f32 v9, v24, v25
	s_waitcnt lgkmcnt(2)
	v_cvt_pk_bf16_f32 v10, v26, v27
	s_waitcnt lgkmcnt(0)
	v_cvt_pk_bf16_f32 v11, v28, v29
	v_lshl_add_u64 v[12:13], v[12:13], 0, v[164:165]
	ds_read_b32 v14, v197
	ds_read_b32 v15, v197 offset:1028
	ds_read_b32 v24, v197 offset:2056
	ds_read_b32 v25, v197 offset:3084
	ds_read_b32 v26, v197 offset:4112
	ds_read_b32 v27, v197 offset:5140
	ds_read_b32 v28, v197 offset:6168
	ds_read_b32 v29, v197 offset:7196
	global_store_dwordx4 v[12:13], v[8:11], off
	v_add_u32_e32 v12, s21, v156
	v_lshlrev_b32_e32 v13, 1, v12
	v_and_b32_e32 v13, 0xffffff00, v13
	v_add_u32_e32 v13, s20, v13
	v_or_b32_e32 v13, v13, v198
	v_cndmask_b32_e32 v12, v13, v12, vcc
	v_mad_i64_i32 v[12:13], s[20:21], s22, v12, 0
	v_lshl_add_u64 v[12:13], v[12:13], 1, s[6:7]
	v_lshl_add_u64 v[12:13], v[12:13], 0, s[4:5]
	s_waitcnt lgkmcnt(6)
	v_cvt_pk_bf16_f32 v8, v14, v15
	s_waitcnt lgkmcnt(4)
	v_cvt_pk_bf16_f32 v9, v24, v25
	s_waitcnt lgkmcnt(2)
	v_cvt_pk_bf16_f32 v10, v26, v27
	s_waitcnt lgkmcnt(0)
	v_cvt_pk_bf16_f32 v11, v28, v29
	v_lshl_add_u64 v[12:13], v[12:13], 0, v[164:165]
	global_store_dwordx4 v[12:13], v[8:11], off
	s_barrier
; #define LAS __attribute__((address_space(3)))
; DI unsigned pk2(float lo, float hi) { f32x2 v = {lo, hi}; return __builtin_bit_cast(unsigned, __builtin_convertvector(v, bf16v2)); }
; DI void conv_store(const ConvItem& c, const f32x4 (&v)[8], LAS float* scr, int tid) {
; #pragma unroll
;     for (int i = 0; i < 8; ++i) { const int idx = tid + 512 * i, row = idx >> 6, c4 = idx & 63; LAS float* d = scr + row * 257 + 4 * c4; d[0] = v[i].x; d[1] = v[i].y; d[2] = v[i].z; d[3] = v[i].w; }
;     __syncthreads();
; #pragma unroll
;     for (int i = 0; i < 4; ++i) { const int idx = tid + 512 * i, n = idx >> 3, cc = idx & 7; const LAS float* sp = scr + (8 * cc) * 257 + n;
;         u32x4 o; o.x = pk2(sp[0], sp[257]); o.y = pk2(sp[2 * 257], sp[3 * 257]); o.z = pk2(sp[4 * 257], sp[5 * 257]); o.w = pk2(sp[6 * 257], sp[7 * 257]);
;         const int h = c.n0 + n; const int drow = (c.mode == 2) ? h : ((h >> 7) * 256 + c.mode * 128 + (h & 127));
;         *(u32x4*)(c.dst + (size_t)drow * c.Kd + c.k0 + 8 * cc) = o; }
;     __syncthreads();
; }
	s_waitcnt vmcnt(15)
	ds_write2_b32 v236, v4, v5 offset1:1
	ds_write2_b32 v236, v6, v7 offset0:2 offset1:3
	s_waitcnt vmcnt(14)
	ds_write2_b32 v237, v0, v1 offset1:1
	ds_write2_b32 v237, v2, v3 offset0:2 offset1:3
	s_waitcnt vmcnt(13)
	ds_write2_b32 v238, v20, v21 offset1:1
	ds_write2_b32 v238, v22, v23 offset0:2 offset1:3
	s_waitcnt vmcnt(12)
	ds_write2_b32 v239, v16, v17 offset1:1
	ds_write2_b32 v239, v18, v19 offset0:2 offset1:3
	s_waitcnt vmcnt(11)
	ds_write2_b32 v240, v36, v37 offset1:1
	ds_write2_b32 v240, v38, v39 offset0:2 offset1:3
	s_waitcnt vmcnt(10)
	ds_write2_b32 v241, v32, v33 offset1:1
	ds_write2_b32 v241, v34, v35 offset0:2 offset1:3
	s_waitcnt vmcnt(9)
	ds_write2_b32 v242, v86, v87 offset1:1
	ds_write2_b32 v242, v88, v89 offset0:2 offset1:3
	s_waitcnt vmcnt(8)
	ds_write2_b32 v243, v82, v83 offset1:1
	ds_write2_b32 v243, v84, v85 offset0:2 offset1:3
	s_waitcnt lgkmcnt(0)
	s_barrier
	ds_read_b32 v0, v188
	ds_read_b32 v1, v188 offset:1028
	ds_read_b32 v2, v188 offset:2056
	ds_read_b32 v3, v188 offset:3084
	ds_read_b32 v4, v188 offset:4112
	ds_read_b32 v5, v188 offset:5140
	ds_read_b32 v6, v188 offset:6168
	ds_read_b32 v7, v188 offset:7196
	s_waitcnt lgkmcnt(6)
	v_cvt_pk_bf16_f32 v0, v0, v1
	s_waitcnt lgkmcnt(4)
	v_cvt_pk_bf16_f32 v1, v2, v3
	s_waitcnt lgkmcnt(2)
	v_cvt_pk_bf16_f32 v2, v4, v5
	v_add_u32_e32 v4, s19, v150
	s_cmp_eq_u32 s23, 2
	v_lshlrev_b32_e32 v5, 1, v4
	s_cselect_b64 vcc, -1, 0
	v_and_b32_e32 v5, 0xffffff00, v5
	s_lshl_b32 s20, s23, 7
	v_add_u32_e32 v5, s20, v5
	v_or_b32_e32 v5, v5, v189
	v_cndmask_b32_e32 v4, v5, v4, vcc
	v_mad_i64_i32 v[4:5], s[4:5], s18, v4, 0
	s_mov_b32 s25, s45
	v_lshl_add_u64 v[4:5], v[4:5], 1, s[2:3]
	s_lshl_b64 s[4:5], s[24:25], 1
	v_lshl_add_u64 v[4:5], v[4:5], 0, s[4:5]
	s_waitcnt lgkmcnt(0)
	v_cvt_pk_bf16_f32 v3, v6, v7
	v_lshl_add_u64 v[4:5], v[4:5], 0, v[164:165]
	ds_read_b32 v6, v191
	ds_read_b32 v7, v191 offset:1028
	ds_read_b32 v8, v191 offset:2056
	ds_read_b32 v9, v191 offset:3084
	ds_read_b32 v10, v191 offset:4112
	ds_read_b32 v11, v191 offset:5140
	ds_read_b32 v12, v191 offset:6168
	ds_read_b32 v13, v191 offset:7196
	global_store_dwordx4 v[4:5], v[0:3], off
	v_add_u32_e32 v4, s19, v152
	v_lshlrev_b32_e32 v5, 1, v4
	v_and_b32_e32 v5, 0xffffff00, v5
	v_add_u32_e32 v5, s20, v5
	v_or_b32_e32 v5, v5, v192
	v_cndmask_b32_e32 v4, v5, v4, vcc
	v_mad_i64_i32 v[4:5], s[6:7], s18, v4, 0
	v_lshl_add_u64 v[4:5], v[4:5], 1, s[2:3]
	v_lshl_add_u64 v[4:5], v[4:5], 0, s[4:5]
	s_waitcnt lgkmcnt(6)
	v_cvt_pk_bf16_f32 v0, v6, v7
	s_waitcnt lgkmcnt(4)
	v_cvt_pk_bf16_f32 v1, v8, v9
	s_waitcnt lgkmcnt(2)
	v_cvt_pk_bf16_f32 v2, v10, v11
	s_waitcnt lgkmcnt(0)
	v_cvt_pk_bf16_f32 v3, v12, v13
	v_lshl_add_u64 v[4:5], v[4:5], 0, v[164:165]
	ds_read_b32 v6, v194
	ds_read_b32 v7, v194 offset:1028
	ds_read_b32 v8, v194 offset:2056
	ds_read_b32 v9, v194 offset:3084
	ds_read_b32 v10, v194 offset:4112
	ds_read_b32 v11, v194 offset:5140
	ds_read_b32 v12, v194 offset:6168
	ds_read_b32 v13, v194 offset:7196
	global_store_dwordx4 v[4:5], v[0:3], off
	v_add_u32_e32 v4, s19, v154
	v_lshlrev_b32_e32 v5, 1, v4
	v_and_b32_e32 v5, 0xffffff00, v5
	v_add_u32_e32 v5, s20, v5
	v_or_b32_e32 v5, v5, v195
	v_cndmask_b32_e32 v4, v5, v4, vcc
	v_mad_i64_i32 v[4:5], s[6:7], s18, v4, 0
	v_lshl_add_u64 v[4:5], v[4:5], 1, s[2:3]
	v_lshl_add_u64 v[4:5], v[4:5], 0, s[4:5]
	s_waitcnt lgkmcnt(6)
	v_cvt_pk_bf16_f32 v0, v6, v7
	s_waitcnt lgkmcnt(4)
	v_cvt_pk_bf16_f32 v1, v8, v9
	s_waitcnt lgkmcnt(2)
	v_cvt_pk_bf16_f32 v2, v10, v11
	s_waitcnt lgkmcnt(0)
	v_cvt_pk_bf16_f32 v3, v12, v13
	v_lshl_add_u64 v[4:5], v[4:5], 0, v[164:165]
	ds_read_b32 v6, v197
	ds_read_b32 v7, v197 offset:1028
	ds_read_b32 v8, v197 offset:2056
	ds_read_b32 v9, v197 offset:3084
	ds_read_b32 v10, v197 offset:4112
	ds_read_b32 v11, v197 offset:5140
	ds_read_b32 v12, v197 offset:6168
	ds_read_b32 v13, v197 offset:7196
	global_store_dwordx4 v[4:5], v[0:3], off
	v_add_u32_e32 v4, s19, v156
	v_lshlrev_b32_e32 v5, 1, v4
	v_and_b32_e32 v5, 0xffffff00, v5
	v_add_u32_e32 v5, s20, v5
	v_or_b32_e32 v5, v5, v198
	v_cndmask_b32_e32 v4, v5, v4, vcc
	v_mad_i64_i32 v[4:5], s[6:7], s18, v4, 0
	v_lshl_add_u64 v[4:5], v[4:5], 1, s[2:3]
	v_lshl_add_u64 v[4:5], v[4:5], 0, s[4:5]
	s_waitcnt lgkmcnt(6)
	v_cvt_pk_bf16_f32 v0, v6, v7
	s_waitcnt lgkmcnt(4)
	v_cvt_pk_bf16_f32 v1, v8, v9
	s_waitcnt lgkmcnt(2)
	v_cvt_pk_bf16_f32 v2, v10, v11
	s_waitcnt lgkmcnt(0)
	v_cvt_pk_bf16_f32 v3, v12, v13
	v_lshl_add_u64 v[4:5], v[4:5], 0, v[164:165]
	s_mov_b64 s[50:51], 0
	global_store_dwordx4 v[4:5], v[0:3], off
	s_barrier
